# speedup vs baseline: 1.0287x; 1.0077x over previous
.LBB1_50:
	v_cvt_pkrtz_f16_f32 v36, v62, v63
	v_cvt_pkrtz_f16_f32 v37, v64, v65
	v_cvt_pkrtz_f16_f32 v38, v66, v67
	v_cvt_pkrtz_f16_f32 v39, v68, v69
	ds_read_b64_tr_b16 v[40:41], v216 offset:32768
	ds_read_b64_tr_b16 v[42:43], v216 offset:33280
	v_add_f32_e32 v34, v62, v63
	v_add_f32_e32 v34, v64, v34
	v_add_f32_e32 v34, v65, v34
	v_add_f32_e32 v34, v66, v34
	ds_read_b64_tr_b16 v[62:63], v216 offset:33792
	ds_read_b64_tr_b16 v[64:65], v216 offset:34304
	s_waitcnt lgkmcnt(2)
	v_mfma_f32_32x32x16_f16 v[2:17], v[36:39], v[40:43], v[2:17]
	ds_read_b64_tr_b16 v[40:41], v216 offset:36864
	ds_read_b64_tr_b16 v[42:43], v216 offset:37376
	v_add_f32_e32 v34, v67, v34
	v_add_f32_e32 v34, v68, v34
	v_add_f32_e32 v34, v69, v34
	v_cvt_pkrtz_f16_f32 v66, v70, v71
	v_cvt_pkrtz_f16_f32 v67, v72, v73
	v_cvt_pkrtz_f16_f32 v68, v74, v75
	v_cvt_pkrtz_f16_f32 v69, v76, v77
	s_waitcnt lgkmcnt(0)
	v_mfma_f32_32x32x16_f16 v[18:33], v[36:39], v[40:43], v[18:33]
	v_add_f32_e32 v34, v70, v34
	v_add_f32_e32 v34, v71, v34
	ds_read_b64_tr_b16 v[78:79], v216 offset:37888
	ds_read_b64_tr_b16 v[80:81], v216 offset:38400
	v_add_f32_e32 v34, v72, v34
	v_add_f32_e32 v34, v73, v34
	v_add_f32_e32 v34, v74, v34
	v_cvt_pkrtz_f16_f32 v36, v46, v47
	v_mfma_f32_32x32x16_f16 v[2:17], v[66:69], v[62:65], v[2:17]
	v_cvt_pkrtz_f16_f32 v37, v48, v49
	v_cvt_pkrtz_f16_f32 v38, v50, v51
	v_cvt_pkrtz_f16_f32 v39, v52, v53
	ds_read_b64_tr_b16 v[40:41], v216 offset:34816
	ds_read_b64_tr_b16 v[42:43], v216 offset:35328
	v_add_f32_e32 v34, v75, v34
	v_add_f32_e32 v34, v76, v34
	v_add_f32_e32 v34, v77, v34
	s_waitcnt lgkmcnt(2)
	v_mfma_f32_32x32x16_f16 v[18:33], v[66:69], v[78:81], v[18:33]
	v_add_f32_e32 v34, v46, v34
	v_add_f32_e32 v34, v47, v34
	ds_read_b64_tr_b16 v[44:45], v216 offset:35840
	ds_read_b64_tr_b16 v[46:47], v216 offset:36352
	v_add_f32_e32 v34, v48, v34
	v_add_f32_e32 v34, v49, v34
	v_add_f32_e32 v34, v50, v34
	v_add_f32_e32 v34, v51, v34
	s_waitcnt lgkmcnt(2)
	v_mfma_f32_32x32x16_f16 v[2:17], v[36:39], v[40:43], v[2:17]
	ds_read_b64_tr_b16 v[40:41], v216 offset:38912
	ds_read_b64_tr_b16 v[42:43], v216 offset:39424
	v_cvt_pkrtz_f16_f32 v48, v54, v55
	ds_read_b64_tr_b16 v[62:63], v216 offset:39936
	ds_read_b64_tr_b16 v[64:65], v216 offset:40448
	v_cvt_pkrtz_f16_f32 v49, v56, v57
	v_cvt_pkrtz_f16_f32 v50, v58, v59
	v_cvt_pkrtz_f16_f32 v51, v60, v61
	v_add_f32_e32 v34, v52, v34
	s_waitcnt lgkmcnt(2)
	v_mfma_f32_32x32x16_f16 v[18:33], v[36:39], v[40:43], v[18:33]
	v_add_f32_e32 v34, v53, v34
	v_add_f32_e32 v34, v54, v34
	v_add_f32_e32 v34, v55, v34
	v_add_f32_e32 v34, v56, v34
	v_add_f32_e32 v34, v57, v34
	v_add_f32_e32 v34, v58, v34
	v_add_f32_e32 v34, v59, v34
	v_mfma_f32_32x32x16_f16 v[2:17], v[48:51], v[44:47], v[2:17]
	v_add_f32_e32 v34, v60, v34
	v_add_f32_e32 v34, v61, v34
	v_add_f32_e32 v34, v35, v34
	v_mov_b32_e32 v35, v34
	s_nop 1
	v_permlane32_swap_b32_e32 v34, v35
	s_waitcnt lgkmcnt(0)
	v_mfma_f32_32x32x16_f16 v[18:33], v[48:51], v[62:65], v[18:33]
	s_and_saveexec_b64 s[6:7], s[4:5]
	v_add_f32_e32 v34, v34, v35
	ds_write_b32 v217, v34 offset:49280
	s_or_b64 exec, exec, s[6:7]
	s_waitcnt lgkmcnt(0)
	ds_read_b128 v[34:37], v204 offset:49280
	ds_read_b128 v[38:41], v204 offset:49312
	s_add_u32 s4, s10, s12
	s_addc_u32 s5, s11, s13
	s_lshl_b32 s6, s24, 12
	s_waitcnt lgkmcnt(1)
	v_rcp_f32_e32 v42, v34
	v_rcp_f32_e32 v43, v35
	s_add_i32 s6, s6, 0
	v_lshlrev_b32_e32 v50, 9, v215
	v_lshlrev_b32_e32 v51, 1, v214
	v_rcp_f32_e32 v44, v36
	v_add3_u32 v50, s6, v50, v51
	v_fma_mixlo_f16 v2, v2, v42, 0
	ds_write_b16 v50, v2 offset:50176
	v_fma_mixlo_f16 v2, v18, v42, 0
	v_rcp_f32_e32 v45, v37
	ds_write_b16 v50, v2 offset:50240
	v_fma_mixlo_f16 v2, v3, v43, 0
	ds_write_b16 v50, v2 offset:50304
	v_fma_mixlo_f16 v2, v19, v43, 0
	s_waitcnt lgkmcnt(3)
	v_rcp_f32_e32 v46, v38
	ds_write_b16 v50, v2 offset:50368
	v_fma_mixlo_f16 v2, v4, v44, 0
	ds_write_b16 v50, v2 offset:50432
	v_fma_mixlo_f16 v2, v20, v44, 0
	v_rcp_f32_e32 v47, v39
	ds_write_b16 v50, v2 offset:50496
	v_fma_mixlo_f16 v2, v5, v45, 0
	ds_read_b128 v[34:37], v204 offset:49344
	ds_write_b16 v50, v2 offset:50560
	v_fma_mixlo_f16 v2, v21, v45, 0
	v_rcp_f32_e32 v48, v40
	ds_write_b16 v50, v2 offset:50624
	v_fma_mixlo_f16 v2, v6, v46, 0
	ds_write_b16 v50, v2 offset:51200
	v_fma_mixlo_f16 v2, v22, v46, 0
	v_rcp_f32_e32 v49, v41
	ds_write_b16 v50, v2 offset:51264
	v_fma_mixlo_f16 v2, v7, v47, 0
	ds_write_b16 v50, v2 offset:51328
	v_fma_mixlo_f16 v2, v23, v47, 0
	ds_read_b128 v[38:41], v204 offset:49376
	s_waitcnt lgkmcnt(6)
	v_rcp_f32_e32 v34, v34
	ds_write_b16 v50, v2 offset:51392
	v_fma_mixlo_f16 v2, v8, v48, 0
	ds_write_b16 v50, v2 offset:51456
	v_fma_mixlo_f16 v2, v24, v48, 0
	v_rcp_f32_e32 v35, v35
	ds_write_b16 v50, v2 offset:51520
	v_fma_mixlo_f16 v2, v9, v49, 0
	ds_write_b16 v50, v2 offset:51584
	v_fma_mixlo_f16 v2, v25, v49, 0
	v_rcp_f32_e32 v36, v36
	ds_write_b16 v50, v2 offset:51648
	v_fma_mixlo_f16 v2, v10, v34, 0
	ds_write_b16 v50, v2 offset:52224
	v_fma_mixlo_f16 v2, v26, v34, 0
	v_rcp_f32_e32 v37, v37
	ds_write_b16 v50, v2 offset:52288
	v_fma_mixlo_f16 v2, v11, v35, 0
	ds_write_b16 v50, v2 offset:52352
	v_fma_mixlo_f16 v2, v27, v35, 0
	s_waitcnt lgkmcnt(8)
	v_rcp_f32_e32 v38, v38
	ds_write_b16 v50, v2 offset:52416
	v_fma_mixlo_f16 v2, v12, v36, 0
	ds_write_b16 v50, v2 offset:52480
	v_fma_mixlo_f16 v2, v28, v36, 0
	v_rcp_f32_e32 v39, v39
	ds_write_b16 v50, v2 offset:52544
	v_fma_mixlo_f16 v2, v13, v37, 0
	ds_write_b16 v50, v2 offset:52608
	v_fma_mixlo_f16 v2, v29, v37, 0
	v_rcp_f32_e32 v40, v40
	ds_write_b16 v50, v2 offset:52672
	v_fma_mixlo_f16 v2, v14, v38, 0
	ds_write_b16 v50, v2 offset:53248
	v_fma_mixlo_f16 v2, v30, v38, 0
	v_rcp_f32_e32 v41, v41
	ds_write_b16 v50, v2 offset:53312
	v_fma_mixlo_f16 v2, v15, v39, 0
	ds_write_b16 v50, v2 offset:53376
	v_fma_mixlo_f16 v2, v31, v39, 0
	ds_write_b16 v50, v2 offset:53440
	v_fma_mixlo_f16 v2, v16, v40, 0
	ds_write_b16 v50, v2 offset:53504
	v_fma_mixlo_f16 v2, v32, v40, 0
	ds_write_b16 v50, v2 offset:53568
	v_fma_mixlo_f16 v2, v17, v41, 0
	ds_write_b16 v50, v2 offset:53632
	v_fma_mixlo_f16 v2, v33, v41, 0
	ds_write_b16 v50, v2 offset:53696
	s_lshl_b32 s3, s3, 1
	v_lshrrev_b32_e32 v10, 3, v212
	v_and_b32_e32 v2, 56, v213
	s_add_u32 s4, s4, s3
	v_lshlrev_b32_e32 v6, 1, v2
	v_lshlrev_b32_e32 v2, 7, v10
	s_addc_u32 s5, s5, 0
	s_waitcnt lgkmcnt(0)
	v_mov_b32_e32 v7, 0
	v_add3_u32 v14, s6, v6, v2
	v_lshl_add_u64 v[8:9], s[4:5], 0, v[6:7]
	ds_read_b128 v[2:5], v14 offset:50176
	v_mul_u32_u24_e32 v6, 0x300, v10
	v_lshlrev_b32_e32 v6, 1, v6
	v_lshl_add_u64 v[10:11], v[8:9], 0, v[6:7]
	ds_read_b128 v[6:9], v14 offset:51200
	s_movk_i32 s3, 0x3000
	s_waitcnt lgkmcnt(1)
	global_store_dwordx4 v[10:11], v[2:5], off sc1
	s_mov_b64 s[4:5], 0
	s_nop 0
	v_add_co_u32_e32 v2, vcc, s3, v10
	s_nop 1
	v_addc_co_u32_e32 v3, vcc, 0, v11, vcc
	s_waitcnt lgkmcnt(0)
	global_store_dwordx4 v[2:3], v[6:9], off sc1
	ds_read_b128 v[2:5], v14 offset:52224
	ds_read_b128 v[6:9], v14 offset:53248
	v_add_co_u32_e32 v12, vcc, 0x6000, v10
	s_nop 1
	v_addc_co_u32_e32 v13, vcc, 0, v11, vcc
	s_waitcnt lgkmcnt(1)
	global_store_dwordx4 v[12:13], v[2:5], off sc1
	s_nop 1
	v_add_co_u32_e32 v2, vcc, 0x9000, v10
	s_nop 1
	v_addc_co_u32_e32 v3, vcc, 0, v11, vcc
	s_waitcnt lgkmcnt(0)
	global_store_dwordx4 v[2:3], v[6:9], off sc1
	s_waitcnt lgkmcnt(0)
	s_barrier

.LBB1_71:
	s_lshl_b64 s[14:15], s[14:15], 1
	s_add_u32 s6, s6, s14
	s_addc_u32 s7, s7, s15
	s_waitcnt lgkmcnt(0)
	v_lshlrev_b32_e32 v8, 1, v16
	v_mov_b32_e32 v9, 0
	v_add_u32_e32 v19, s12, v4
	v_lshl_add_u64 v[8:9], s[6:7], 0, v[8:9]
	v_mad_u64_u32 v[10:11], s[6:7], s4, v19, 0
	v_mov_b32_e32 v12, v11
	v_mad_u64_u32 v[12:13], s[6:7], s5, v19, v[12:13]
	v_mov_b32_e32 v11, v12
	v_lshl_add_u64 v[20:21], v[10:11], 1, v[8:9]
	v_add_u32_e32 v10, 0x400, v18
	ds_read2_b32 v[16:17], v18 offset0:32 offset1:97
	ds_read2_b32 v[14:15], v18 offset0:162 offset1:227
	ds_read2_b32 v[12:13], v10 offset0:36 offset1:101
	ds_read2_b32 v[10:11], v10 offset0:166 offset1:231
	s_andn2_b64 vcc, exec, s[10:11]
	global_store_dwordx4 v[20:21], v[0:3], off sc1
	s_cbranch_vccnz .LBB1_73
	s_waitcnt lgkmcnt(3)
	v_cvt_pk_f16_f32 v0, v16, v17
	s_waitcnt lgkmcnt(2)
	v_cvt_pk_f16_f32 v1, v14, v15
	s_waitcnt lgkmcnt(1)
	v_cvt_pk_f16_f32 v2, v12, v13
	s_waitcnt lgkmcnt(0)
	v_cvt_pk_f16_f32 v3, v10, v11
	s_cbranch_execz .LBB1_74
	s_branch .LBB1_77

.LBB1_77:
	s_waitcnt lgkmcnt(1)
	v_add_u32_e32 v7, 32, v19
	v_mad_u64_u32 v[4:5], s[0:1], s4, v7, 0
	v_mov_b32_e32 v6, v5
	v_mad_u64_u32 v[6:7], s[0:1], s5, v7, v[6:7]
	v_mov_b32_e32 v5, v6
	v_lshl_add_u64 v[4:5], v[4:5], 1, v[8:9]
	global_store_dwordx4 v[4:5], v[0:3], off sc1
	s_endpgm

_Z6gemm_kILi1ELb1ELb1ELb0ELb0ELb1EEvPKtS1_ii7EpiArgs:
	s_load_dwordx8 s[4:11], s[0:1], 0x0
	s_load_dwordx2 s[14:15], s[0:1], 0x30
	s_load_dwordx2 s[12:13], s[0:1], 0x48
	s_lshl_b32 s0, s2, 3
	s_and_b32 s0, s0, 56
	s_bfe_u32 s1, s2, 0x30003
	s_or_b32 s0, s0, s1
	s_lshl_b32 s22, s0, 7
	v_readfirstlane_b32 s18, v0
	s_lshr_b32 s1, s2, 6
	s_waitcnt lgkmcnt(0)
	s_mul_hi_i32 s3, s9, s22
	s_mul_i32 s2, s9, s22
	s_lshr_b32 s19, s18, 6
	s_bfe_u32 s23, s18, 0x20006
	s_ashr_i32 s17, s9, 31
	s_lshl_b64 s[2:3], s[2:3], 1
	s_mul_i32 s0, s1, 0xc0
	s_add_u32 s2, s4, s2
	s_addc_u32 s3, s5, s3
	s_mul_hi_i32 s5, s9, s0
	s_mul_i32 s4, s9, s0
	s_ashr_i32 s1, s0, 31
	s_lshl_b64 s[4:5], s[4:5], 1
	s_add_u32 s4, s6, s4
	v_lshrrev_b32_e32 v1, 4, v0
	s_addc_u32 s5, s7, s5
	s_lshr_b32 s6, s18, 2
	v_xor_b32_e32 v4, v1, v0
	s_lshl_b32 s25, s19, 10
	s_and_b32 s6, s6, 0x3fffffc0
	v_and_b32_e32 v2, 15, v0
	v_lshrrev_b32_e32 v3, 3, v0
	v_lshlrev_b32_e32 v4, 3, v4
	v_bfe_u32 v5, v0, 1, 3
	s_cmp_lg_u32 0, -1
	v_mul_lo_u32 v3, s9, v3
	v_and_b32_e32 v4, 56, v4
	s_mov_b32 s16, s9
	v_bitop3_b32 v5, v1, v5, 3 bitop3:0x6c
	v_or_b32_e32 v1, s6, v2
	s_cselect_b32 s6, 0, 0
	v_add_lshl_u32 v84, v3, v4, 1
	s_add_i32 s25, s25, s6
	s_nop 4
	s_mov_b32 s6, m0
	s_mov_b32 m0, s25
	s_nop 0
	global_load_lds_dwordx4 v84, s[2:3] nt
	s_mov_b32 m0, s6
	s_lshl_b64 s[18:19], s[16:17], 7
	s_add_u32 s6, s2, s18
	s_addc_u32 s7, s3, s19
	s_add_i32 s26, s25, 0x2000
	s_nop 4
	s_mov_b32 s16, m0
	s_mov_b32 m0, s26
	s_nop 0
	global_load_lds_dwordx4 v84, s[6:7] nt
	s_mov_b32 m0, s16
	s_add_i32 s27, s25, 0x4000
	s_nop 4
	s_mov_b32 s16, m0
	s_mov_b32 m0, s27
	s_nop 0
	global_load_lds_dwordx4 v84, s[4:5]
	s_mov_b32 m0, s16
	s_add_u32 s16, s4, s18
	s_addc_u32 s17, s5, s19
	s_add_i32 s28, s25, 0x6000
	s_nop 4
	s_mov_b32 s20, m0
	s_mov_b32 m0, s28
	s_nop 0
	global_load_lds_dwordx4 v84, s[16:17]
	s_mov_b32 m0, s20
	s_add_u32 s18, s16, s18
	s_addc_u32 s19, s17, s19
	s_add_i32 s29, s25, 0x8000
	s_nop 4
	s_mov_b32 s20, m0
	s_mov_b32 m0, s29
	s_nop 0
	global_load_lds_dwordx4 v84, s[18:19]
	s_mov_b32 m0, s20
	s_add_u32 s20, s2, 0x80
	s_addc_u32 s21, s3, 0
	s_add_i32 s30, s25, 0xa000
	s_nop 4
	s_mov_b32 s31, m0
	s_mov_b32 m0, s30
	s_nop 0
	global_load_lds_dwordx4 v84, s[20:21] nt
	s_mov_b32 m0, s31
	s_add_u32 s20, s6, 0x80
	s_addc_u32 s21, s7, 0
	s_add_i32 s31, s25, 0xc000
	s_nop 4
	s_mov_b32 s33, m0
	s_mov_b32 m0, s31
	s_nop 0
	global_load_lds_dwordx4 v84, s[20:21] nt
	s_mov_b32 m0, s33
	s_add_u32 s20, s4, 0x80
	s_addc_u32 s21, s5, 0
	s_add_i32 s33, s25, 0xe000
	s_nop 4
	s_mov_b32 s34, m0
	s_mov_b32 m0, s33
	s_nop 0
	global_load_lds_dwordx4 v84, s[20:21]
	s_mov_b32 m0, s34
	s_add_u32 s20, s16, 0x80
	s_addc_u32 s21, s17, 0
	s_add_i32 s34, s25, 0x10000
	s_nop 4
	s_mov_b32 s35, m0
	s_mov_b32 m0, s34
	s_nop 0
	global_load_lds_dwordx4 v84, s[20:21]
	s_mov_b32 m0, s35
	s_add_u32 s20, s18, 0x80
	s_addc_u32 s21, s19, 0
	s_add_i32 s35, s25, 0x12000
	s_nop 4
	s_mov_b32 s36, m0
	s_mov_b32 m0, s35
	s_nop 0
	global_load_lds_dwordx4 v84, s[20:21]
	s_mov_b32 m0, s36
	s_add_u32 s20, s2, 0x100
	s_addc_u32 s21, s3, 0
	s_add_i32 s36, s25, 0x14000
	s_nop 4
	s_mov_b32 s37, m0
	s_mov_b32 m0, s36
	s_nop 0
	global_load_lds_dwordx4 v84, s[20:21] nt
	s_mov_b32 m0, s37
	s_add_u32 s20, s6, 0x100
	s_addc_u32 s21, s7, 0
	s_add_i32 s37, s25, 0x16000
	s_nop 4
	s_mov_b32 s38, m0
	s_mov_b32 m0, s37
	s_nop 0
	global_load_lds_dwordx4 v84, s[20:21] nt
	s_mov_b32 m0, s38
	s_add_u32 s20, s4, 0x100
	s_addc_u32 s21, s5, 0
	s_add_i32 s38, s25, 0x18000
	s_nop 4
	s_mov_b32 s39, m0
	s_mov_b32 m0, s38
	s_nop 0
	global_load_lds_dwordx4 v84, s[20:21]
	s_mov_b32 m0, s39
	s_add_u32 s20, s16, 0x100
	s_addc_u32 s21, s17, 0
	s_add_i32 s39, s25, 0x1a000
	s_mul_i32 s23, s23, 48
	s_nop 4
	s_mov_b32 s40, m0
	s_mov_b32 m0, s39
	s_nop 0
	global_load_lds_dwordx4 v84, s[20:21]
	s_mov_b32 m0, s40
	s_add_u32 s20, s18, 0x100
	v_lshlrev_b32_e32 v5, 4, v5
	v_or_b32_e32 v2, s23, v2
	v_lshl_add_u32 v31, v1, 7, 0
	s_addc_u32 s21, s19, 0
	s_add_i32 s40, s25, 0x1c000
	s_nop 4
	s_mov_b32 s41, m0
	s_mov_b32 m0, s40
	s_nop 0
	global_load_lds_dwordx4 v84, s[20:21]
	s_mov_b32 m0, s41
	v_xor_b32_e32 v30, 64, v5
	v_lshl_add_u32 v2, v2, 7, 0
	v_add_u32_e32 v79, v31, v5
	s_waitcnt vmcnt(10) lgkmcnt(0)
	s_barrier
	v_add_u32_e32 v82, v2, v5
	v_add_u32_e32 v81, v2, v30
	s_ashr_i32 s9, s9, 6
	v_add_u32_e32 v83, v31, v30
	s_mul_i32 s70, s22, s8
	s_add_u32 s70, s70, s0
	s_lshl_b32 s71, s70, 1
	s_add_u32 s72, s12, s71
	s_addc_u32 s73, s13, 0
	s_lshl_b32 s71, s70, 2
	s_add_u32 s74, s10, s71
	s_addc_u32 s75, s11, 0
	s_movk_i32 s76, 0xffd0
	v_add_u32_e32 v100, 0x14000, v79
	v_add_u32_e32 v101, 0x14000, v83
	v_add_u32_e32 v102, 0x14000, v82
	v_add_u32_e32 v103, 0x14000, v81
	s_add_u32 s54, s2, 0x100
	s_addc_u32 s55, s3, 0
	s_add_u32 s56, s6, 0x100
	s_addc_u32 s57, s7, 0
	s_add_u32 s58, s4, 0x100
	s_addc_u32 s59, s5, 0
	s_add_u32 s60, s16, 0x100
	s_addc_u32 s61, s17, 0
	s_add_u32 s62, s18, 0x100
	s_addc_u32 s63, s19, 0
	s_mul_hi_u32 s64, s9, 0x55555556
	s_add_i32 s64, s64, -1
	ds_read_b128 v[168:171], v79 offset:0
	ds_read_b128 v[184:187], v82 offset:16384
	ds_read_b128 v[188:191], v82 offset:18432
	ds_read_b128 v[192:195], v82 offset:20480
	ds_read_b128 v[172:175], v79 offset:2048
	ds_read_b128 v[176:179], v79 offset:4096
	ds_read_b128 v[180:183], v79 offset:6144
	v_mov_b32_e32 v120, 0
	v_mov_b32_e32 v121, 0
	v_mov_b32_e32 v122, 0
	v_mov_b32_e32 v123, 0
	v_mov_b32_e32 v124, 0
	v_mov_b32_e32 v125, 0
	v_mov_b32_e32 v126, 0
	v_mov_b32_e32 v127, 0
	v_mov_b32_e32 v128, 0
	v_mov_b32_e32 v129, 0
	v_mov_b32_e32 v130, 0
	v_mov_b32_e32 v131, 0
	v_mov_b32_e32 v132, 0
	v_mov_b32_e32 v133, 0
	v_mov_b32_e32 v134, 0
	v_mov_b32_e32 v135, 0
	v_mov_b32_e32 v136, 0
	v_mov_b32_e32 v137, 0
	v_mov_b32_e32 v138, 0
	v_mov_b32_e32 v139, 0
	v_mov_b32_e32 v140, 0
	v_mov_b32_e32 v141, 0
	v_mov_b32_e32 v142, 0
	v_mov_b32_e32 v143, 0
	v_mov_b32_e32 v144, 0
	v_mov_b32_e32 v145, 0
	v_mov_b32_e32 v146, 0
	v_mov_b32_e32 v147, 0
	v_mov_b32_e32 v148, 0
	v_mov_b32_e32 v149, 0
	v_mov_b32_e32 v150, 0
	v_mov_b32_e32 v151, 0
	v_mov_b32_e32 v152, 0
	v_mov_b32_e32 v153, 0
	v_mov_b32_e32 v154, 0
	v_mov_b32_e32 v155, 0
	v_mov_b32_e32 v156, 0
	v_mov_b32_e32 v157, 0
	v_mov_b32_e32 v158, 0
	v_mov_b32_e32 v159, 0
	v_mov_b32_e32 v160, 0
	v_mov_b32_e32 v161, 0
	v_mov_b32_e32 v162, 0
	v_mov_b32_e32 v163, 0
	v_mov_b32_e32 v164, 0
	v_mov_b32_e32 v165, 0
	v_mov_b32_e32 v166, 0
	v_mov_b32_e32 v167, 0
	s_waitcnt lgkmcnt(0)
	v_mfma_f32_16x16x32_f16 v[120:123], v[184:187], v[168:171], v[120:123]
	ds_read_b128 v[196:199], v83 offset:0
	v_mfma_f32_16x16x32_f16 v[124:127], v[188:191], v[168:171], v[124:127]
	ds_read_b128 v[212:215], v81 offset:16384
	v_mfma_f32_16x16x32_f16 v[128:131], v[192:195], v[168:171], v[128:131]
	ds_read_b128 v[216:219], v81 offset:18432
	v_mfma_f32_16x16x32_f16 v[132:135], v[184:187], v[172:175], v[132:135]
	ds_read_b128 v[220:223], v81 offset:20480
	v_mfma_f32_16x16x32_f16 v[136:139], v[188:191], v[172:175], v[136:139]
	ds_read_b128 v[200:203], v83 offset:2048
	v_mfma_f32_16x16x32_f16 v[140:143], v[192:195], v[172:175], v[140:143]
	ds_read_b128 v[204:207], v83 offset:4096
	v_mfma_f32_16x16x32_f16 v[144:147], v[184:187], v[176:179], v[144:147]
	ds_read_b128 v[208:211], v83 offset:6144
	v_mfma_f32_16x16x32_f16 v[148:151], v[188:191], v[176:179], v[148:151]
	v_mfma_f32_16x16x32_f16 v[152:155], v[192:195], v[176:179], v[152:155]
	v_mfma_f32_16x16x32_f16 v[156:159], v[184:187], v[180:183], v[156:159]
	v_mfma_f32_16x16x32_f16 v[160:163], v[188:191], v[180:183], v[160:163]
	v_mfma_f32_16x16x32_f16 v[164:167], v[192:195], v[180:183], v[164:167]
	s_cmp_ge_u32 s25, 0x1000
	s_cbranch_scc1 .Lgk_loop_dnB
.Lgk_loop_dnA:
	s_waitcnt vmcnt(5) lgkmcnt(0)
	s_barrier
	s_mov_b32 m0, s25
	s_add_u32 s54, s54, 0x80
	s_addc_u32 s55, s55, 0
	global_load_lds_dwordx4 v84, s[54:55]
	s_mov_b32 m0, s26
	s_add_u32 s56, s56, 0x80
	s_addc_u32 s57, s57, 0
	global_load_lds_dwordx4 v84, s[56:57]
	s_mov_b32 m0, s27
	s_add_u32 s58, s58, 0x80
	s_addc_u32 s59, s59, 0
	global_load_lds_dwordx4 v84, s[58:59]
	s_mov_b32 m0, s28
	s_add_u32 s60, s60, 0x80
	s_addc_u32 s61, s61, 0
	global_load_lds_dwordx4 v84, s[60:61]
	s_mov_b32 m0, s29
	s_add_u32 s62, s62, 0x80
	s_addc_u32 s63, s63, 0
	global_load_lds_dwordx4 v84, s[62:63]
	v_mfma_f32_16x16x32_f16 v[120:123], v[212:215], v[196:199], v[120:123]
	ds_read_b128 v[168:171], v79 offset:40960
	v_mfma_f32_16x16x32_f16 v[124:127], v[216:219], v[196:199], v[124:127]
	ds_read_b128 v[184:187], v82 offset:57344
	v_mfma_f32_16x16x32_f16 v[128:131], v[220:223], v[196:199], v[128:131]
	ds_read_b128 v[188:191], v82 offset:59392
	v_mfma_f32_16x16x32_f16 v[132:135], v[212:215], v[200:203], v[132:135]
	ds_read_b128 v[192:195], v82 offset:61440
	v_mfma_f32_16x16x32_f16 v[136:139], v[216:219], v[200:203], v[136:139]
	ds_read_b128 v[172:175], v79 offset:43008
	v_mfma_f32_16x16x32_f16 v[140:143], v[220:223], v[200:203], v[140:143]
	ds_read_b128 v[176:179], v79 offset:45056
	v_mfma_f32_16x16x32_f16 v[144:147], v[212:215], v[204:207], v[144:147]
	ds_read_b128 v[180:183], v79 offset:47104
	v_mfma_f32_16x16x32_f16 v[148:151], v[216:219], v[204:207], v[148:151]
	v_mfma_f32_16x16x32_f16 v[152:155], v[220:223], v[204:207], v[152:155]
	v_mfma_f32_16x16x32_f16 v[156:159], v[212:215], v[208:211], v[156:159]
	v_mfma_f32_16x16x32_f16 v[160:163], v[216:219], v[208:211], v[160:163]
	v_mfma_f32_16x16x32_f16 v[164:167], v[220:223], v[208:211], v[164:167]
	s_waitcnt lgkmcnt(0)
	v_mfma_f32_16x16x32_f16 v[120:123], v[184:187], v[168:171], v[120:123]
	ds_read_b128 v[196:199], v83 offset:40960
	v_mfma_f32_16x16x32_f16 v[124:127], v[188:191], v[168:171], v[124:127]
	ds_read_b128 v[212:215], v81 offset:57344
	v_mfma_f32_16x16x32_f16 v[128:131], v[192:195], v[168:171], v[128:131]
	ds_read_b128 v[216:219], v81 offset:59392
	v_mfma_f32_16x16x32_f16 v[132:135], v[184:187], v[172:175], v[132:135]
	ds_read_b128 v[220:223], v81 offset:61440
	v_mfma_f32_16x16x32_f16 v[136:139], v[188:191], v[172:175], v[136:139]
	ds_read_b128 v[200:203], v83 offset:43008
	v_mfma_f32_16x16x32_f16 v[140:143], v[192:195], v[172:175], v[140:143]
	ds_read_b128 v[204:207], v83 offset:45056
	v_mfma_f32_16x16x32_f16 v[144:147], v[184:187], v[176:179], v[144:147]
	ds_read_b128 v[208:211], v83 offset:47104
	v_mfma_f32_16x16x32_f16 v[148:151], v[188:191], v[176:179], v[148:151]
	v_mfma_f32_16x16x32_f16 v[152:155], v[192:195], v[176:179], v[152:155]
	v_mfma_f32_16x16x32_f16 v[156:159], v[184:187], v[180:183], v[156:159]
	v_mfma_f32_16x16x32_f16 v[160:163], v[188:191], v[180:183], v[160:163]
	v_mfma_f32_16x16x32_f16 v[164:167], v[192:195], v[180:183], v[164:167]
	s_waitcnt vmcnt(5) lgkmcnt(0)
	s_barrier
	s_mov_b32 m0, s30
	s_add_u32 s54, s54, 0x80
	s_addc_u32 s55, s55, 0
	global_load_lds_dwordx4 v84, s[54:55]
	s_mov_b32 m0, s31
	s_add_u32 s56, s56, 0x80
	s_addc_u32 s57, s57, 0
	global_load_lds_dwordx4 v84, s[56:57]
	s_mov_b32 m0, s33
	s_add_u32 s58, s58, 0x80
	s_addc_u32 s59, s59, 0
	global_load_lds_dwordx4 v84, s[58:59]
	s_mov_b32 m0, s34
	s_add_u32 s60, s60, 0x80
	s_addc_u32 s61, s61, 0
	global_load_lds_dwordx4 v84, s[60:61]
	s_mov_b32 m0, s35
	s_add_u32 s62, s62, 0x80
	s_addc_u32 s63, s63, 0
	global_load_lds_dwordx4 v84, s[62:63]
	v_mfma_f32_16x16x32_f16 v[120:123], v[212:215], v[196:199], v[120:123]
	ds_read_b128 v[168:171], v100 offset:0
	v_mfma_f32_16x16x32_f16 v[124:127], v[216:219], v[196:199], v[124:127]
	ds_read_b128 v[184:187], v102 offset:16384
	v_mfma_f32_16x16x32_f16 v[128:131], v[220:223], v[196:199], v[128:131]
	ds_read_b128 v[188:191], v102 offset:18432
	v_mfma_f32_16x16x32_f16 v[132:135], v[212:215], v[200:203], v[132:135]
	ds_read_b128 v[192:195], v102 offset:20480
	v_mfma_f32_16x16x32_f16 v[136:139], v[216:219], v[200:203], v[136:139]
	ds_read_b128 v[172:175], v100 offset:2048
	v_mfma_f32_16x16x32_f16 v[140:143], v[220:223], v[200:203], v[140:143]
	ds_read_b128 v[176:179], v100 offset:4096
	v_mfma_f32_16x16x32_f16 v[144:147], v[212:215], v[204:207], v[144:147]
	ds_read_b128 v[180:183], v100 offset:6144
	v_mfma_f32_16x16x32_f16 v[148:151], v[216:219], v[204:207], v[148:151]
	v_mfma_f32_16x16x32_f16 v[152:155], v[220:223], v[204:207], v[152:155]
	v_mfma_f32_16x16x32_f16 v[156:159], v[212:215], v[208:211], v[156:159]
	v_mfma_f32_16x16x32_f16 v[160:163], v[216:219], v[208:211], v[160:163]
	v_mfma_f32_16x16x32_f16 v[164:167], v[220:223], v[208:211], v[164:167]
	s_waitcnt lgkmcnt(0)
	v_mfma_f32_16x16x32_f16 v[120:123], v[184:187], v[168:171], v[120:123]
	ds_read_b128 v[196:199], v101 offset:0
	v_mfma_f32_16x16x32_f16 v[124:127], v[188:191], v[168:171], v[124:127]
	ds_read_b128 v[212:215], v103 offset:16384
	v_mfma_f32_16x16x32_f16 v[128:131], v[192:195], v[168:171], v[128:131]
	ds_read_b128 v[216:219], v103 offset:18432
	v_mfma_f32_16x16x32_f16 v[132:135], v[184:187], v[172:175], v[132:135]
	ds_read_b128 v[220:223], v103 offset:20480
	v_mfma_f32_16x16x32_f16 v[136:139], v[188:191], v[172:175], v[136:139]
	ds_read_b128 v[200:203], v101 offset:2048
	v_mfma_f32_16x16x32_f16 v[140:143], v[192:195], v[172:175], v[140:143]
	ds_read_b128 v[204:207], v101 offset:4096
	v_mfma_f32_16x16x32_f16 v[144:147], v[184:187], v[176:179], v[144:147]
	ds_read_b128 v[208:211], v101 offset:6144
	v_mfma_f32_16x16x32_f16 v[148:151], v[188:191], v[176:179], v[148:151]
	v_mfma_f32_16x16x32_f16 v[152:155], v[192:195], v[176:179], v[152:155]
	v_mfma_f32_16x16x32_f16 v[156:159], v[184:187], v[180:183], v[156:159]
	v_mfma_f32_16x16x32_f16 v[160:163], v[188:191], v[180:183], v[160:163]
	v_mfma_f32_16x16x32_f16 v[164:167], v[192:195], v[180:183], v[164:167]
	s_waitcnt vmcnt(5) lgkmcnt(0)
	s_barrier
	s_mov_b32 m0, s36
	s_add_u32 s54, s54, 0x80
	s_addc_u32 s55, s55, 0
	global_load_lds_dwordx4 v84, s[54:55]
	s_mov_b32 m0, s37
	s_add_u32 s56, s56, 0x80
	s_addc_u32 s57, s57, 0
	global_load_lds_dwordx4 v84, s[56:57]
	s_mov_b32 m0, s38
	s_add_u32 s58, s58, 0x80
	s_addc_u32 s59, s59, 0
	global_load_lds_dwordx4 v84, s[58:59]
	s_mov_b32 m0, s39
	s_add_u32 s60, s60, 0x80
	s_addc_u32 s61, s61, 0
	global_load_lds_dwordx4 v84, s[60:61]
	s_mov_b32 m0, s40
	s_add_u32 s62, s62, 0x80
	s_addc_u32 s63, s63, 0
	global_load_lds_dwordx4 v84, s[62:63]
	v_mfma_f32_16x16x32_f16 v[120:123], v[212:215], v[196:199], v[120:123]
	ds_read_b128 v[168:171], v79 offset:0
	v_mfma_f32_16x16x32_f16 v[124:127], v[216:219], v[196:199], v[124:127]
	ds_read_b128 v[184:187], v82 offset:16384
	v_mfma_f32_16x16x32_f16 v[128:131], v[220:223], v[196:199], v[128:131]
	ds_read_b128 v[188:191], v82 offset:18432
	v_mfma_f32_16x16x32_f16 v[132:135], v[212:215], v[200:203], v[132:135]
	ds_read_b128 v[192:195], v82 offset:20480
	v_mfma_f32_16x16x32_f16 v[136:139], v[216:219], v[200:203], v[136:139]
	ds_read_b128 v[172:175], v79 offset:2048
	v_mfma_f32_16x16x32_f16 v[140:143], v[220:223], v[200:203], v[140:143]
	ds_read_b128 v[176:179], v79 offset:4096
	v_mfma_f32_16x16x32_f16 v[144:147], v[212:215], v[204:207], v[144:147]
	ds_read_b128 v[180:183], v79 offset:6144
	v_mfma_f32_16x16x32_f16 v[148:151], v[216:219], v[204:207], v[148:151]
	v_mfma_f32_16x16x32_f16 v[152:155], v[220:223], v[204:207], v[152:155]
	v_mfma_f32_16x16x32_f16 v[156:159], v[212:215], v[208:211], v[156:159]
	v_mfma_f32_16x16x32_f16 v[160:163], v[216:219], v[208:211], v[160:163]
	v_mfma_f32_16x16x32_f16 v[164:167], v[220:223], v[208:211], v[164:167]
	s_waitcnt lgkmcnt(0)
	v_mfma_f32_16x16x32_f16 v[120:123], v[184:187], v[168:171], v[120:123]
	ds_read_b128 v[196:199], v83 offset:0
	v_mfma_f32_16x16x32_f16 v[124:127], v[188:191], v[168:171], v[124:127]
	ds_read_b128 v[212:215], v81 offset:16384
	v_mfma_f32_16x16x32_f16 v[128:131], v[192:195], v[168:171], v[128:131]
	ds_read_b128 v[216:219], v81 offset:18432
	v_mfma_f32_16x16x32_f16 v[132:135], v[184:187], v[172:175], v[132:135]
	ds_read_b128 v[220:223], v81 offset:20480
	v_mfma_f32_16x16x32_f16 v[136:139], v[188:191], v[172:175], v[136:139]
	ds_read_b128 v[200:203], v83 offset:2048
	v_mfma_f32_16x16x32_f16 v[140:143], v[192:195], v[172:175], v[140:143]
	ds_read_b128 v[204:207], v83 offset:4096
	v_mfma_f32_16x16x32_f16 v[144:147], v[184:187], v[176:179], v[144:147]
	ds_read_b128 v[208:211], v83 offset:6144
	v_mfma_f32_16x16x32_f16 v[148:151], v[188:191], v[176:179], v[148:151]
	v_mfma_f32_16x16x32_f16 v[152:155], v[192:195], v[176:179], v[152:155]
	v_mfma_f32_16x16x32_f16 v[156:159], v[184:187], v[180:183], v[156:159]
	v_mfma_f32_16x16x32_f16 v[160:163], v[188:191], v[180:183], v[160:163]
	v_mfma_f32_16x16x32_f16 v[164:167], v[192:195], v[180:183], v[164:167]
	s_add_i32 s64, s64, -1
	s_cmp_lg_u32 s64, 0
	s_cbranch_scc1 .Lgk_loop_dnA
	v_mov_b32_e32 v50, v0
	v_mul_u32_u24_e32 v51, 0xaab, v50
	v_lshrrev_b32_e32 v51, 17, v51
	v_mad_i32_i24 v52, v51, s76, v50
	v_mul_u32_u24_e32 v26, 0x300, v51
	v_lshl_add_u32 v26, v52, 2, v26
	v_mul_u32_u24_e32 v38, 0x310, v51
	v_lshl_add_u32 v38, v52, 4, v38
	v_lshlrev_b32_e32 v50, 1, v26
	global_load_dwordx2 v[2:3], v50, s[72:73] nt
	v_or_b32_e32 v50, 512, v0
	v_mul_u32_u24_e32 v51, 0xaab, v50
	v_lshrrev_b32_e32 v51, 17, v51
	v_mad_i32_i24 v52, v51, s76, v50
	v_mul_u32_u24_e32 v27, 0x300, v51
	v_lshl_add_u32 v27, v52, 2, v27
	v_mul_u32_u24_e32 v39, 0x310, v51
	v_lshl_add_u32 v39, v52, 4, v39
	v_lshlrev_b32_e32 v50, 1, v27
	global_load_dwordx2 v[4:5], v50, s[72:73] nt
	v_or_b32_e32 v50, 1024, v0
	v_mul_u32_u24_e32 v51, 0xaab, v50
	v_lshrrev_b32_e32 v51, 17, v51
	v_mad_i32_i24 v52, v51, s76, v50
	v_mul_u32_u24_e32 v28, 0x300, v51
	v_lshl_add_u32 v28, v52, 2, v28
	v_mul_u32_u24_e32 v40, 0x310, v51
	v_lshl_add_u32 v40, v52, 4, v40
	v_lshlrev_b32_e32 v50, 1, v28
	global_load_dwordx2 v[6:7], v50, s[72:73] nt
	v_or_b32_e32 v50, 1536, v0
	v_mul_u32_u24_e32 v51, 0xaab, v50
	v_lshrrev_b32_e32 v51, 17, v51
	v_mad_i32_i24 v52, v51, s76, v50
	v_mul_u32_u24_e32 v29, 0x300, v51
	v_lshl_add_u32 v29, v52, 2, v29
	v_mul_u32_u24_e32 v41, 0x310, v51
	v_lshl_add_u32 v41, v52, 4, v41
	v_lshlrev_b32_e32 v50, 1, v29
	global_load_dwordx2 v[8:9], v50, s[72:73] nt
	v_or_b32_e32 v50, 2048, v0
	v_mul_u32_u24_e32 v51, 0xaab, v50
	v_lshrrev_b32_e32 v51, 17, v51
	v_mad_i32_i24 v52, v51, s76, v50
	v_mul_u32_u24_e32 v30, 0x300, v51
	v_lshl_add_u32 v30, v52, 2, v30
	v_mul_u32_u24_e32 v42, 0x310, v51
	v_lshl_add_u32 v42, v52, 4, v42
	v_lshlrev_b32_e32 v50, 1, v30
	global_load_dwordx2 v[10:11], v50, s[72:73] nt
	v_or_b32_e32 v50, 2560, v0
	v_mul_u32_u24_e32 v51, 0xaab, v50
	v_lshrrev_b32_e32 v51, 17, v51
	v_mad_i32_i24 v52, v51, s76, v50
	v_mul_u32_u24_e32 v31, 0x300, v51
	v_lshl_add_u32 v31, v52, 2, v31
	v_mul_u32_u24_e32 v43, 0x310, v51
	v_lshl_add_u32 v43, v52, 4, v43
	v_lshlrev_b32_e32 v50, 1, v31
	global_load_dwordx2 v[12:13], v50, s[72:73] nt
	v_or_b32_e32 v50, 3072, v0
	v_mul_u32_u24_e32 v51, 0xaab, v50
	v_lshrrev_b32_e32 v51, 17, v51
	v_mad_i32_i24 v52, v51, s76, v50
	v_mul_u32_u24_e32 v32, 0x300, v51
	v_lshl_add_u32 v32, v52, 2, v32
	v_mul_u32_u24_e32 v44, 0x310, v51
	v_lshl_add_u32 v44, v52, 4, v44
	v_lshlrev_b32_e32 v50, 1, v32
	global_load_dwordx2 v[14:15], v50, s[72:73] nt
	v_or_b32_e32 v50, 3584, v0
	v_mul_u32_u24_e32 v51, 0xaab, v50
	v_lshrrev_b32_e32 v51, 17, v51
	v_mad_i32_i24 v52, v51, s76, v50
	v_mul_u32_u24_e32 v33, 0x300, v51
	v_lshl_add_u32 v33, v52, 2, v33
	v_mul_u32_u24_e32 v45, 0x310, v51
	v_lshl_add_u32 v45, v52, 4, v45
	v_lshlrev_b32_e32 v50, 1, v33
	global_load_dwordx2 v[16:17], v50, s[72:73] nt
	v_or_b32_e32 v50, 4096, v0
	v_mul_u32_u24_e32 v51, 0xaab, v50
	v_lshrrev_b32_e32 v51, 17, v51
	v_mad_i32_i24 v52, v51, s76, v50
	v_mul_u32_u24_e32 v34, 0x300, v51
	v_lshl_add_u32 v34, v52, 2, v34
	v_mul_u32_u24_e32 v46, 0x310, v51
	v_lshl_add_u32 v46, v52, 4, v46
	v_lshlrev_b32_e32 v50, 1, v34
	global_load_dwordx2 v[18:19], v50, s[72:73] nt
	v_or_b32_e32 v50, 4608, v0
	v_mul_u32_u24_e32 v51, 0xaab, v50
	v_lshrrev_b32_e32 v51, 17, v51
	v_mad_i32_i24 v52, v51, s76, v50
	v_mul_u32_u24_e32 v35, 0x300, v51
	v_lshl_add_u32 v35, v52, 2, v35
	v_mul_u32_u24_e32 v47, 0x310, v51
	v_lshl_add_u32 v47, v52, 4, v47
	v_lshlrev_b32_e32 v50, 1, v35
	global_load_dwordx2 v[20:21], v50, s[72:73] nt
	v_or_b32_e32 v50, 5120, v0
	v_mul_u32_u24_e32 v51, 0xaab, v50
	v_lshrrev_b32_e32 v51, 17, v51
	v_mad_i32_i24 v52, v51, s76, v50
	v_mul_u32_u24_e32 v36, 0x300, v51
	v_lshl_add_u32 v36, v52, 2, v36
	v_mul_u32_u24_e32 v48, 0x310, v51
	v_lshl_add_u32 v48, v52, 4, v48
	v_lshlrev_b32_e32 v50, 1, v36
	global_load_dwordx2 v[22:23], v50, s[72:73] nt
	v_or_b32_e32 v50, 5632, v0
	v_mul_u32_u24_e32 v51, 0xaab, v50
	v_lshrrev_b32_e32 v51, 17, v51
	v_mad_i32_i24 v52, v51, s76, v50
	v_mul_u32_u24_e32 v37, 0x300, v51
	v_lshl_add_u32 v37, v52, 2, v37
	v_mul_u32_u24_e32 v49, 0x310, v51
	v_lshl_add_u32 v49, v52, 4, v49
	v_lshlrev_b32_e32 v50, 1, v37
	global_load_dwordx2 v[24:25], v50, s[72:73] nt
	s_waitcnt vmcnt(17) lgkmcnt(0)
	s_barrier
	v_mfma_f32_16x16x32_f16 v[120:123], v[212:215], v[196:199], v[120:123]
	ds_read_b128 v[168:171], v79 offset:40960
	v_mfma_f32_16x16x32_f16 v[124:127], v[216:219], v[196:199], v[124:127]
	ds_read_b128 v[184:187], v82 offset:57344
	v_mfma_f32_16x16x32_f16 v[128:131], v[220:223], v[196:199], v[128:131]
	ds_read_b128 v[188:191], v82 offset:59392
	v_mfma_f32_16x16x32_f16 v[132:135], v[212:215], v[200:203], v[132:135]
	ds_read_b128 v[192:195], v82 offset:61440
	v_mfma_f32_16x16x32_f16 v[136:139], v[216:219], v[200:203], v[136:139]
	ds_read_b128 v[172:175], v79 offset:43008
	v_mfma_f32_16x16x32_f16 v[140:143], v[220:223], v[200:203], v[140:143]
	ds_read_b128 v[176:179], v79 offset:45056
	v_mfma_f32_16x16x32_f16 v[144:147], v[212:215], v[204:207], v[144:147]
	ds_read_b128 v[180:183], v79 offset:47104
	v_mfma_f32_16x16x32_f16 v[148:151], v[216:219], v[204:207], v[148:151]
	v_mfma_f32_16x16x32_f16 v[152:155], v[220:223], v[204:207], v[152:155]
	v_mfma_f32_16x16x32_f16 v[156:159], v[212:215], v[208:211], v[156:159]
	v_mfma_f32_16x16x32_f16 v[160:163], v[216:219], v[208:211], v[160:163]
	v_mfma_f32_16x16x32_f16 v[164:167], v[220:223], v[208:211], v[164:167]
	s_waitcnt lgkmcnt(0)
	v_mfma_f32_16x16x32_f16 v[120:123], v[184:187], v[168:171], v[120:123]
	ds_read_b128 v[196:199], v83 offset:40960
	v_mfma_f32_16x16x32_f16 v[124:127], v[188:191], v[168:171], v[124:127]
	ds_read_b128 v[212:215], v81 offset:57344
	v_mfma_f32_16x16x32_f16 v[128:131], v[192:195], v[168:171], v[128:131]
	ds_read_b128 v[216:219], v81 offset:59392
	v_mfma_f32_16x16x32_f16 v[132:135], v[184:187], v[172:175], v[132:135]
	ds_read_b128 v[220:223], v81 offset:61440
	v_mfma_f32_16x16x32_f16 v[136:139], v[188:191], v[172:175], v[136:139]
	ds_read_b128 v[200:203], v83 offset:43008
	v_mfma_f32_16x16x32_f16 v[140:143], v[192:195], v[172:175], v[140:143]
	ds_read_b128 v[204:207], v83 offset:45056
	v_mfma_f32_16x16x32_f16 v[144:147], v[184:187], v[176:179], v[144:147]
	ds_read_b128 v[208:211], v83 offset:47104
	v_mfma_f32_16x16x32_f16 v[148:151], v[188:191], v[176:179], v[148:151]
	v_mfma_f32_16x16x32_f16 v[152:155], v[192:195], v[176:179], v[152:155]
	v_mfma_f32_16x16x32_f16 v[156:159], v[184:187], v[180:183], v[156:159]
	v_mfma_f32_16x16x32_f16 v[160:163], v[188:191], v[180:183], v[160:163]
	v_mfma_f32_16x16x32_f16 v[164:167], v[192:195], v[180:183], v[164:167]
	s_waitcnt vmcnt(12) lgkmcnt(0)
	s_barrier
	v_mfma_f32_16x16x32_f16 v[120:123], v[212:215], v[196:199], v[120:123]
	ds_read_b128 v[168:171], v100 offset:0
	v_mfma_f32_16x16x32_f16 v[124:127], v[216:219], v[196:199], v[124:127]
	ds_read_b128 v[184:187], v102 offset:16384
	v_mfma_f32_16x16x32_f16 v[128:131], v[220:223], v[196:199], v[128:131]
	ds_read_b128 v[188:191], v102 offset:18432
	v_mfma_f32_16x16x32_f16 v[132:135], v[212:215], v[200:203], v[132:135]
	ds_read_b128 v[192:195], v102 offset:20480
	v_mfma_f32_16x16x32_f16 v[136:139], v[216:219], v[200:203], v[136:139]
	ds_read_b128 v[172:175], v100 offset:2048
	v_mfma_f32_16x16x32_f16 v[140:143], v[220:223], v[200:203], v[140:143]
	ds_read_b128 v[176:179], v100 offset:4096
	v_mfma_f32_16x16x32_f16 v[144:147], v[212:215], v[204:207], v[144:147]
	ds_read_b128 v[180:183], v100 offset:6144
	v_mfma_f32_16x16x32_f16 v[148:151], v[216:219], v[204:207], v[148:151]
	v_mfma_f32_16x16x32_f16 v[152:155], v[220:223], v[204:207], v[152:155]
	v_mfma_f32_16x16x32_f16 v[156:159], v[212:215], v[208:211], v[156:159]
	v_mfma_f32_16x16x32_f16 v[160:163], v[216:219], v[208:211], v[160:163]
	v_mfma_f32_16x16x32_f16 v[164:167], v[220:223], v[208:211], v[164:167]
	s_waitcnt lgkmcnt(0)
	v_mfma_f32_16x16x32_f16 v[120:123], v[184:187], v[168:171], v[120:123]
	ds_read_b128 v[196:199], v101 offset:0
	v_mfma_f32_16x16x32_f16 v[124:127], v[188:191], v[168:171], v[124:127]
	ds_read_b128 v[212:215], v103 offset:16384
	v_mfma_f32_16x16x32_f16 v[128:131], v[192:195], v[168:171], v[128:131]
	ds_read_b128 v[216:219], v103 offset:18432
	v_mfma_f32_16x16x32_f16 v[132:135], v[184:187], v[172:175], v[132:135]
	ds_read_b128 v[220:223], v103 offset:20480
	v_mfma_f32_16x16x32_f16 v[136:139], v[188:191], v[172:175], v[136:139]
	ds_read_b128 v[200:203], v101 offset:2048
	v_mfma_f32_16x16x32_f16 v[140:143], v[192:195], v[172:175], v[140:143]
	ds_read_b128 v[204:207], v101 offset:4096
	v_mfma_f32_16x16x32_f16 v[144:147], v[184:187], v[176:179], v[144:147]
	ds_read_b128 v[208:211], v101 offset:6144
	v_mfma_f32_16x16x32_f16 v[148:151], v[188:191], v[176:179], v[148:151]
	v_mfma_f32_16x16x32_f16 v[152:155], v[192:195], v[176:179], v[152:155]
	v_mfma_f32_16x16x32_f16 v[156:159], v[184:187], v[180:183], v[156:159]
	v_mfma_f32_16x16x32_f16 v[160:163], v[188:191], v[180:183], v[160:163]
	v_mfma_f32_16x16x32_f16 v[164:167], v[192:195], v[180:183], v[164:167]
	s_waitcnt lgkmcnt(0)
	v_mfma_f32_16x16x32_f16 v[120:123], v[212:215], v[196:199], v[120:123]
	v_mfma_f32_16x16x32_f16 v[124:127], v[216:219], v[196:199], v[124:127]
	v_mfma_f32_16x16x32_f16 v[128:131], v[220:223], v[196:199], v[128:131]
	v_mfma_f32_16x16x32_f16 v[132:135], v[212:215], v[200:203], v[132:135]
	v_mfma_f32_16x16x32_f16 v[136:139], v[216:219], v[200:203], v[136:139]
	v_mfma_f32_16x16x32_f16 v[140:143], v[220:223], v[200:203], v[140:143]
	v_mfma_f32_16x16x32_f16 v[144:147], v[212:215], v[204:207], v[144:147]
	v_mfma_f32_16x16x32_f16 v[148:151], v[216:219], v[204:207], v[148:151]
	v_mfma_f32_16x16x32_f16 v[152:155], v[220:223], v[204:207], v[152:155]
	v_mfma_f32_16x16x32_f16 v[156:159], v[212:215], v[208:211], v[156:159]
	v_mfma_f32_16x16x32_f16 v[160:163], v[216:219], v[208:211], v[160:163]
	v_mfma_f32_16x16x32_f16 v[164:167], v[220:223], v[208:211], v[164:167]
	s_branch .Lgk_loop_dn_done
.Lgk_loop_dnB:
	s_waitcnt vmcnt(5) lgkmcnt(0)
	s_barrier
	v_mfma_f32_16x16x32_f16 v[120:123], v[212:215], v[196:199], v[120:123]
	ds_read_b128 v[168:171], v79 offset:40960
	v_mfma_f32_16x16x32_f16 v[124:127], v[216:219], v[196:199], v[124:127]
	ds_read_b128 v[184:187], v82 offset:57344
	v_mfma_f32_16x16x32_f16 v[128:131], v[220:223], v[196:199], v[128:131]
	ds_read_b128 v[188:191], v82 offset:59392
	v_mfma_f32_16x16x32_f16 v[132:135], v[212:215], v[200:203], v[132:135]
	ds_read_b128 v[192:195], v82 offset:61440
	v_mfma_f32_16x16x32_f16 v[136:139], v[216:219], v[200:203], v[136:139]
	ds_read_b128 v[172:175], v79 offset:43008
	v_mfma_f32_16x16x32_f16 v[140:143], v[220:223], v[200:203], v[140:143]
	ds_read_b128 v[176:179], v79 offset:45056
	v_mfma_f32_16x16x32_f16 v[144:147], v[212:215], v[204:207], v[144:147]
	ds_read_b128 v[180:183], v79 offset:47104
	v_mfma_f32_16x16x32_f16 v[148:151], v[216:219], v[204:207], v[148:151]
	v_mfma_f32_16x16x32_f16 v[152:155], v[220:223], v[204:207], v[152:155]
	v_mfma_f32_16x16x32_f16 v[156:159], v[212:215], v[208:211], v[156:159]
	v_mfma_f32_16x16x32_f16 v[160:163], v[216:219], v[208:211], v[160:163]
	v_mfma_f32_16x16x32_f16 v[164:167], v[220:223], v[208:211], v[164:167]
	s_waitcnt lgkmcnt(0)
	v_mfma_f32_16x16x32_f16 v[120:123], v[184:187], v[168:171], v[120:123]
	ds_read_b128 v[196:199], v83 offset:40960
	v_mfma_f32_16x16x32_f16 v[124:127], v[188:191], v[168:171], v[124:127]
	ds_read_b128 v[212:215], v81 offset:57344
	v_mfma_f32_16x16x32_f16 v[128:131], v[192:195], v[168:171], v[128:131]
	ds_read_b128 v[216:219], v81 offset:59392
	v_mfma_f32_16x16x32_f16 v[132:135], v[184:187], v[172:175], v[132:135]
	ds_read_b128 v[220:223], v81 offset:61440
	v_mfma_f32_16x16x32_f16 v[136:139], v[188:191], v[172:175], v[136:139]
	ds_read_b128 v[200:203], v83 offset:43008
	v_mfma_f32_16x16x32_f16 v[140:143], v[192:195], v[172:175], v[140:143]
	ds_read_b128 v[204:207], v83 offset:45056
	v_mfma_f32_16x16x32_f16 v[144:147], v[184:187], v[176:179], v[144:147]
	ds_read_b128 v[208:211], v83 offset:47104
	v_mfma_f32_16x16x32_f16 v[148:151], v[188:191], v[176:179], v[148:151]
	v_mfma_f32_16x16x32_f16 v[152:155], v[192:195], v[176:179], v[152:155]
	v_mfma_f32_16x16x32_f16 v[156:159], v[184:187], v[180:183], v[156:159]
	v_mfma_f32_16x16x32_f16 v[160:163], v[188:191], v[180:183], v[160:163]
	v_mfma_f32_16x16x32_f16 v[164:167], v[192:195], v[180:183], v[164:167]
	s_mov_b32 m0, s25
	s_add_u32 s54, s54, 0x80
	s_addc_u32 s55, s55, 0
	global_load_lds_dwordx4 v84, s[54:55]
	s_mov_b32 m0, s26
	s_add_u32 s56, s56, 0x80
	s_addc_u32 s57, s57, 0
	global_load_lds_dwordx4 v84, s[56:57]
	s_mov_b32 m0, s27
	s_add_u32 s58, s58, 0x80
	s_addc_u32 s59, s59, 0
	global_load_lds_dwordx4 v84, s[58:59]
	s_mov_b32 m0, s28
	s_add_u32 s60, s60, 0x80
	s_addc_u32 s61, s61, 0
	global_load_lds_dwordx4 v84, s[60:61]
	s_mov_b32 m0, s29
	s_add_u32 s62, s62, 0x80
	s_addc_u32 s63, s63, 0
	global_load_lds_dwordx4 v84, s[62:63]
	s_waitcnt vmcnt(5) lgkmcnt(0)
	s_barrier
	v_mfma_f32_16x16x32_f16 v[120:123], v[212:215], v[196:199], v[120:123]
	ds_read_b128 v[168:171], v100 offset:0
	v_mfma_f32_16x16x32_f16 v[124:127], v[216:219], v[196:199], v[124:127]
	ds_read_b128 v[184:187], v102 offset:16384
	v_mfma_f32_16x16x32_f16 v[128:131], v[220:223], v[196:199], v[128:131]
	ds_read_b128 v[188:191], v102 offset:18432
	v_mfma_f32_16x16x32_f16 v[132:135], v[212:215], v[200:203], v[132:135]
	ds_read_b128 v[192:195], v102 offset:20480
	v_mfma_f32_16x16x32_f16 v[136:139], v[216:219], v[200:203], v[136:139]
	ds_read_b128 v[172:175], v100 offset:2048
	v_mfma_f32_16x16x32_f16 v[140:143], v[220:223], v[200:203], v[140:143]
	ds_read_b128 v[176:179], v100 offset:4096
	v_mfma_f32_16x16x32_f16 v[144:147], v[212:215], v[204:207], v[144:147]
	ds_read_b128 v[180:183], v100 offset:6144
	v_mfma_f32_16x16x32_f16 v[148:151], v[216:219], v[204:207], v[148:151]
	v_mfma_f32_16x16x32_f16 v[152:155], v[220:223], v[204:207], v[152:155]
	v_mfma_f32_16x16x32_f16 v[156:159], v[212:215], v[208:211], v[156:159]
	v_mfma_f32_16x16x32_f16 v[160:163], v[216:219], v[208:211], v[160:163]
	v_mfma_f32_16x16x32_f16 v[164:167], v[220:223], v[208:211], v[164:167]
	s_waitcnt lgkmcnt(0)
	v_mfma_f32_16x16x32_f16 v[120:123], v[184:187], v[168:171], v[120:123]
	ds_read_b128 v[196:199], v101 offset:0
	v_mfma_f32_16x16x32_f16 v[124:127], v[188:191], v[168:171], v[124:127]
	ds_read_b128 v[212:215], v103 offset:16384
	v_mfma_f32_16x16x32_f16 v[128:131], v[192:195], v[168:171], v[128:131]
	ds_read_b128 v[216:219], v103 offset:18432
	v_mfma_f32_16x16x32_f16 v[132:135], v[184:187], v[172:175], v[132:135]
	ds_read_b128 v[220:223], v103 offset:20480
	v_mfma_f32_16x16x32_f16 v[136:139], v[188:191], v[172:175], v[136:139]
	ds_read_b128 v[200:203], v101 offset:2048
	v_mfma_f32_16x16x32_f16 v[140:143], v[192:195], v[172:175], v[140:143]
	ds_read_b128 v[204:207], v101 offset:4096
	v_mfma_f32_16x16x32_f16 v[144:147], v[184:187], v[176:179], v[144:147]
	ds_read_b128 v[208:211], v101 offset:6144
	v_mfma_f32_16x16x32_f16 v[148:151], v[188:191], v[176:179], v[148:151]
	v_mfma_f32_16x16x32_f16 v[152:155], v[192:195], v[176:179], v[152:155]
	v_mfma_f32_16x16x32_f16 v[156:159], v[184:187], v[180:183], v[156:159]
	v_mfma_f32_16x16x32_f16 v[160:163], v[188:191], v[180:183], v[160:163]
	v_mfma_f32_16x16x32_f16 v[164:167], v[192:195], v[180:183], v[164:167]
	s_mov_b32 m0, s30
	s_add_u32 s54, s54, 0x80
	s_addc_u32 s55, s55, 0
	global_load_lds_dwordx4 v84, s[54:55]
	s_mov_b32 m0, s31
	s_add_u32 s56, s56, 0x80
	s_addc_u32 s57, s57, 0
	global_load_lds_dwordx4 v84, s[56:57]
	s_mov_b32 m0, s33
	s_add_u32 s58, s58, 0x80
	s_addc_u32 s59, s59, 0
	global_load_lds_dwordx4 v84, s[58:59]
	s_mov_b32 m0, s34
	s_add_u32 s60, s60, 0x80
	s_addc_u32 s61, s61, 0
	global_load_lds_dwordx4 v84, s[60:61]
	s_mov_b32 m0, s35
	s_add_u32 s62, s62, 0x80
	s_addc_u32 s63, s63, 0
	global_load_lds_dwordx4 v84, s[62:63]
	s_waitcnt vmcnt(5) lgkmcnt(0)
	s_barrier
	v_mfma_f32_16x16x32_f16 v[120:123], v[212:215], v[196:199], v[120:123]
	ds_read_b128 v[168:171], v79 offset:0
	v_mfma_f32_16x16x32_f16 v[124:127], v[216:219], v[196:199], v[124:127]
	ds_read_b128 v[184:187], v82 offset:16384
	v_mfma_f32_16x16x32_f16 v[128:131], v[220:223], v[196:199], v[128:131]
	ds_read_b128 v[188:191], v82 offset:18432
	v_mfma_f32_16x16x32_f16 v[132:135], v[212:215], v[200:203], v[132:135]
	ds_read_b128 v[192:195], v82 offset:20480
	v_mfma_f32_16x16x32_f16 v[136:139], v[216:219], v[200:203], v[136:139]
	ds_read_b128 v[172:175], v79 offset:2048
	v_mfma_f32_16x16x32_f16 v[140:143], v[220:223], v[200:203], v[140:143]
	ds_read_b128 v[176:179], v79 offset:4096
	v_mfma_f32_16x16x32_f16 v[144:147], v[212:215], v[204:207], v[144:147]
	ds_read_b128 v[180:183], v79 offset:6144
	v_mfma_f32_16x16x32_f16 v[148:151], v[216:219], v[204:207], v[148:151]
	v_mfma_f32_16x16x32_f16 v[152:155], v[220:223], v[204:207], v[152:155]
	v_mfma_f32_16x16x32_f16 v[156:159], v[212:215], v[208:211], v[156:159]
	v_mfma_f32_16x16x32_f16 v[160:163], v[216:219], v[208:211], v[160:163]
	v_mfma_f32_16x16x32_f16 v[164:167], v[220:223], v[208:211], v[164:167]
	s_waitcnt lgkmcnt(0)
	v_mfma_f32_16x16x32_f16 v[120:123], v[184:187], v[168:171], v[120:123]
	ds_read_b128 v[196:199], v83 offset:0
	v_mfma_f32_16x16x32_f16 v[124:127], v[188:191], v[168:171], v[124:127]
	ds_read_b128 v[212:215], v81 offset:16384
	v_mfma_f32_16x16x32_f16 v[128:131], v[192:195], v[168:171], v[128:131]
	ds_read_b128 v[216:219], v81 offset:18432
	v_mfma_f32_16x16x32_f16 v[132:135], v[184:187], v[172:175], v[132:135]
	ds_read_b128 v[220:223], v81 offset:20480
	v_mfma_f32_16x16x32_f16 v[136:139], v[188:191], v[172:175], v[136:139]
	ds_read_b128 v[200:203], v83 offset:2048
	v_mfma_f32_16x16x32_f16 v[140:143], v[192:195], v[172:175], v[140:143]
	ds_read_b128 v[204:207], v83 offset:4096
	v_mfma_f32_16x16x32_f16 v[144:147], v[184:187], v[176:179], v[144:147]
	ds_read_b128 v[208:211], v83 offset:6144
	v_mfma_f32_16x16x32_f16 v[148:151], v[188:191], v[176:179], v[148:151]
	v_mfma_f32_16x16x32_f16 v[152:155], v[192:195], v[176:179], v[152:155]
	v_mfma_f32_16x16x32_f16 v[156:159], v[184:187], v[180:183], v[156:159]
	v_mfma_f32_16x16x32_f16 v[160:163], v[188:191], v[180:183], v[160:163]
	v_mfma_f32_16x16x32_f16 v[164:167], v[192:195], v[180:183], v[164:167]
	s_mov_b32 m0, s36
	s_add_u32 s54, s54, 0x80
	s_addc_u32 s55, s55, 0
	global_load_lds_dwordx4 v84, s[54:55]
	s_mov_b32 m0, s37
	s_add_u32 s56, s56, 0x80
	s_addc_u32 s57, s57, 0
	global_load_lds_dwordx4 v84, s[56:57]
	s_mov_b32 m0, s38
	s_add_u32 s58, s58, 0x80
	s_addc_u32 s59, s59, 0
	global_load_lds_dwordx4 v84, s[58:59]
	s_mov_b32 m0, s39
	s_add_u32 s60, s60, 0x80
	s_addc_u32 s61, s61, 0
	global_load_lds_dwordx4 v84, s[60:61]
	s_mov_b32 m0, s40
	s_add_u32 s62, s62, 0x80
	s_addc_u32 s63, s63, 0
	global_load_lds_dwordx4 v84, s[62:63]
	s_add_i32 s64, s64, -1
	s_cmp_lg_u32 s64, 0
	s_cbranch_scc1 .Lgk_loop_dnB
	v_mov_b32_e32 v50, v0
	v_mul_u32_u24_e32 v51, 0xaab, v50
	v_lshrrev_b32_e32 v51, 17, v51
	v_mad_i32_i24 v52, v51, s76, v50
	v_mul_u32_u24_e32 v26, 0x300, v51
	v_lshl_add_u32 v26, v52, 2, v26
	v_mul_u32_u24_e32 v38, 0x310, v51
	v_lshl_add_u32 v38, v52, 4, v38
	v_lshlrev_b32_e32 v50, 1, v26
	global_load_dwordx2 v[2:3], v50, s[72:73] nt
	v_or_b32_e32 v50, 512, v0
	v_mul_u32_u24_e32 v51, 0xaab, v50
	v_lshrrev_b32_e32 v51, 17, v51
	v_mad_i32_i24 v52, v51, s76, v50
	v_mul_u32_u24_e32 v27, 0x300, v51
	v_lshl_add_u32 v27, v52, 2, v27
	v_mul_u32_u24_e32 v39, 0x310, v51
	v_lshl_add_u32 v39, v52, 4, v39
	v_lshlrev_b32_e32 v50, 1, v27
	global_load_dwordx2 v[4:5], v50, s[72:73] nt
	v_or_b32_e32 v50, 1024, v0
	v_mul_u32_u24_e32 v51, 0xaab, v50
	v_lshrrev_b32_e32 v51, 17, v51
	v_mad_i32_i24 v52, v51, s76, v50
	v_mul_u32_u24_e32 v28, 0x300, v51
	v_lshl_add_u32 v28, v52, 2, v28
	v_mul_u32_u24_e32 v40, 0x310, v51
	v_lshl_add_u32 v40, v52, 4, v40
	v_lshlrev_b32_e32 v50, 1, v28
	global_load_dwordx2 v[6:7], v50, s[72:73] nt
	v_or_b32_e32 v50, 1536, v0
	v_mul_u32_u24_e32 v51, 0xaab, v50
	v_lshrrev_b32_e32 v51, 17, v51
	v_mad_i32_i24 v52, v51, s76, v50
	v_mul_u32_u24_e32 v29, 0x300, v51
	v_lshl_add_u32 v29, v52, 2, v29
	v_mul_u32_u24_e32 v41, 0x310, v51
	v_lshl_add_u32 v41, v52, 4, v41
	v_lshlrev_b32_e32 v50, 1, v29
	global_load_dwordx2 v[8:9], v50, s[72:73] nt
	v_or_b32_e32 v50, 2048, v0
	v_mul_u32_u24_e32 v51, 0xaab, v50
	v_lshrrev_b32_e32 v51, 17, v51
	v_mad_i32_i24 v52, v51, s76, v50
	v_mul_u32_u24_e32 v30, 0x300, v51
	v_lshl_add_u32 v30, v52, 2, v30
	v_mul_u32_u24_e32 v42, 0x310, v51
	v_lshl_add_u32 v42, v52, 4, v42
	v_lshlrev_b32_e32 v50, 1, v30
	global_load_dwordx2 v[10:11], v50, s[72:73] nt
	v_or_b32_e32 v50, 2560, v0
	v_mul_u32_u24_e32 v51, 0xaab, v50
	v_lshrrev_b32_e32 v51, 17, v51
	v_mad_i32_i24 v52, v51, s76, v50
	v_mul_u32_u24_e32 v31, 0x300, v51
	v_lshl_add_u32 v31, v52, 2, v31
	v_mul_u32_u24_e32 v43, 0x310, v51
	v_lshl_add_u32 v43, v52, 4, v43
	v_lshlrev_b32_e32 v50, 1, v31
	global_load_dwordx2 v[12:13], v50, s[72:73] nt
	v_or_b32_e32 v50, 3072, v0
	v_mul_u32_u24_e32 v51, 0xaab, v50
	v_lshrrev_b32_e32 v51, 17, v51
	v_mad_i32_i24 v52, v51, s76, v50
	v_mul_u32_u24_e32 v32, 0x300, v51
	v_lshl_add_u32 v32, v52, 2, v32
	v_mul_u32_u24_e32 v44, 0x310, v51
	v_lshl_add_u32 v44, v52, 4, v44
	v_lshlrev_b32_e32 v50, 1, v32
	global_load_dwordx2 v[14:15], v50, s[72:73] nt
	v_or_b32_e32 v50, 3584, v0
	v_mul_u32_u24_e32 v51, 0xaab, v50
	v_lshrrev_b32_e32 v51, 17, v51
	v_mad_i32_i24 v52, v51, s76, v50
	v_mul_u32_u24_e32 v33, 0x300, v51
	v_lshl_add_u32 v33, v52, 2, v33
	v_mul_u32_u24_e32 v45, 0x310, v51
	v_lshl_add_u32 v45, v52, 4, v45
	v_lshlrev_b32_e32 v50, 1, v33
	global_load_dwordx2 v[16:17], v50, s[72:73] nt
	v_or_b32_e32 v50, 4096, v0
	v_mul_u32_u24_e32 v51, 0xaab, v50
	v_lshrrev_b32_e32 v51, 17, v51
	v_mad_i32_i24 v52, v51, s76, v50
	v_mul_u32_u24_e32 v34, 0x300, v51
	v_lshl_add_u32 v34, v52, 2, v34
	v_mul_u32_u24_e32 v46, 0x310, v51
	v_lshl_add_u32 v46, v52, 4, v46
	v_lshlrev_b32_e32 v50, 1, v34
	global_load_dwordx2 v[18:19], v50, s[72:73] nt
	v_or_b32_e32 v50, 4608, v0
	v_mul_u32_u24_e32 v51, 0xaab, v50
	v_lshrrev_b32_e32 v51, 17, v51
	v_mad_i32_i24 v52, v51, s76, v50
	v_mul_u32_u24_e32 v35, 0x300, v51
	v_lshl_add_u32 v35, v52, 2, v35
	v_mul_u32_u24_e32 v47, 0x310, v51
	v_lshl_add_u32 v47, v52, 4, v47
	v_lshlrev_b32_e32 v50, 1, v35
	global_load_dwordx2 v[20:21], v50, s[72:73] nt
	v_or_b32_e32 v50, 5120, v0
	v_mul_u32_u24_e32 v51, 0xaab, v50
	v_lshrrev_b32_e32 v51, 17, v51
	v_mad_i32_i24 v52, v51, s76, v50
	v_mul_u32_u24_e32 v36, 0x300, v51
	v_lshl_add_u32 v36, v52, 2, v36
	v_mul_u32_u24_e32 v48, 0x310, v51
	v_lshl_add_u32 v48, v52, 4, v48
	v_lshlrev_b32_e32 v50, 1, v36
	global_load_dwordx2 v[22:23], v50, s[72:73] nt
	v_or_b32_e32 v50, 5632, v0
	v_mul_u32_u24_e32 v51, 0xaab, v50
	v_lshrrev_b32_e32 v51, 17, v51
	v_mad_i32_i24 v52, v51, s76, v50
	v_mul_u32_u24_e32 v37, 0x300, v51
	v_lshl_add_u32 v37, v52, 2, v37
	v_mul_u32_u24_e32 v49, 0x310, v51
	v_lshl_add_u32 v49, v52, 4, v49
	v_lshlrev_b32_e32 v50, 1, v37
	global_load_dwordx2 v[24:25], v50, s[72:73] nt
	s_waitcnt vmcnt(17) lgkmcnt(0)
	s_barrier
	v_mfma_f32_16x16x32_f16 v[120:123], v[212:215], v[196:199], v[120:123]
	ds_read_b128 v[168:171], v79 offset:40960
	v_mfma_f32_16x16x32_f16 v[124:127], v[216:219], v[196:199], v[124:127]
	ds_read_b128 v[184:187], v82 offset:57344
	v_mfma_f32_16x16x32_f16 v[128:131], v[220:223], v[196:199], v[128:131]
	ds_read_b128 v[188:191], v82 offset:59392
	v_mfma_f32_16x16x32_f16 v[132:135], v[212:215], v[200:203], v[132:135]
	ds_read_b128 v[192:195], v82 offset:61440
	v_mfma_f32_16x16x32_f16 v[136:139], v[216:219], v[200:203], v[136:139]
	ds_read_b128 v[172:175], v79 offset:43008
	v_mfma_f32_16x16x32_f16 v[140:143], v[220:223], v[200:203], v[140:143]
	ds_read_b128 v[176:179], v79 offset:45056
	v_mfma_f32_16x16x32_f16 v[144:147], v[212:215], v[204:207], v[144:147]
	ds_read_b128 v[180:183], v79 offset:47104
	v_mfma_f32_16x16x32_f16 v[148:151], v[216:219], v[204:207], v[148:151]
	v_mfma_f32_16x16x32_f16 v[152:155], v[220:223], v[204:207], v[152:155]
	v_mfma_f32_16x16x32_f16 v[156:159], v[212:215], v[208:211], v[156:159]
	v_mfma_f32_16x16x32_f16 v[160:163], v[216:219], v[208:211], v[160:163]
	v_mfma_f32_16x16x32_f16 v[164:167], v[220:223], v[208:211], v[164:167]
	s_waitcnt lgkmcnt(0)
	v_mfma_f32_16x16x32_f16 v[120:123], v[184:187], v[168:171], v[120:123]
	ds_read_b128 v[196:199], v83 offset:40960
	v_mfma_f32_16x16x32_f16 v[124:127], v[188:191], v[168:171], v[124:127]
	ds_read_b128 v[212:215], v81 offset:57344
	v_mfma_f32_16x16x32_f16 v[128:131], v[192:195], v[168:171], v[128:131]
	ds_read_b128 v[216:219], v81 offset:59392
	v_mfma_f32_16x16x32_f16 v[132:135], v[184:187], v[172:175], v[132:135]
	ds_read_b128 v[220:223], v81 offset:61440
	v_mfma_f32_16x16x32_f16 v[136:139], v[188:191], v[172:175], v[136:139]
	ds_read_b128 v[200:203], v83 offset:43008
	v_mfma_f32_16x16x32_f16 v[140:143], v[192:195], v[172:175], v[140:143]
	ds_read_b128 v[204:207], v83 offset:45056
	v_mfma_f32_16x16x32_f16 v[144:147], v[184:187], v[176:179], v[144:147]
	ds_read_b128 v[208:211], v83 offset:47104
	v_mfma_f32_16x16x32_f16 v[148:151], v[188:191], v[176:179], v[148:151]
	v_mfma_f32_16x16x32_f16 v[152:155], v[192:195], v[176:179], v[152:155]
	v_mfma_f32_16x16x32_f16 v[156:159], v[184:187], v[180:183], v[156:159]
	v_mfma_f32_16x16x32_f16 v[160:163], v[188:191], v[180:183], v[160:163]
	v_mfma_f32_16x16x32_f16 v[164:167], v[192:195], v[180:183], v[164:167]
	s_waitcnt vmcnt(12) lgkmcnt(0)
	s_barrier
	v_mfma_f32_16x16x32_f16 v[120:123], v[212:215], v[196:199], v[120:123]
	ds_read_b128 v[168:171], v100 offset:0
	v_mfma_f32_16x16x32_f16 v[124:127], v[216:219], v[196:199], v[124:127]
	ds_read_b128 v[184:187], v102 offset:16384
	v_mfma_f32_16x16x32_f16 v[128:131], v[220:223], v[196:199], v[128:131]
	ds_read_b128 v[188:191], v102 offset:18432
	v_mfma_f32_16x16x32_f16 v[132:135], v[212:215], v[200:203], v[132:135]
	ds_read_b128 v[192:195], v102 offset:20480
	v_mfma_f32_16x16x32_f16 v[136:139], v[216:219], v[200:203], v[136:139]
	ds_read_b128 v[172:175], v100 offset:2048
	v_mfma_f32_16x16x32_f16 v[140:143], v[220:223], v[200:203], v[140:143]
	ds_read_b128 v[176:179], v100 offset:4096
	v_mfma_f32_16x16x32_f16 v[144:147], v[212:215], v[204:207], v[144:147]
	ds_read_b128 v[180:183], v100 offset:6144
	v_mfma_f32_16x16x32_f16 v[148:151], v[216:219], v[204:207], v[148:151]
	v_mfma_f32_16x16x32_f16 v[152:155], v[220:223], v[204:207], v[152:155]
	v_mfma_f32_16x16x32_f16 v[156:159], v[212:215], v[208:211], v[156:159]
	v_mfma_f32_16x16x32_f16 v[160:163], v[216:219], v[208:211], v[160:163]
	v_mfma_f32_16x16x32_f16 v[164:167], v[220:223], v[208:211], v[164:167]
	s_waitcnt lgkmcnt(0)
	v_mfma_f32_16x16x32_f16 v[120:123], v[184:187], v[168:171], v[120:123]
	ds_read_b128 v[196:199], v101 offset:0
	v_mfma_f32_16x16x32_f16 v[124:127], v[188:191], v[168:171], v[124:127]
	ds_read_b128 v[212:215], v103 offset:16384
	v_mfma_f32_16x16x32_f16 v[128:131], v[192:195], v[168:171], v[128:131]
	ds_read_b128 v[216:219], v103 offset:18432
	v_mfma_f32_16x16x32_f16 v[132:135], v[184:187], v[172:175], v[132:135]
	ds_read_b128 v[220:223], v103 offset:20480
	v_mfma_f32_16x16x32_f16 v[136:139], v[188:191], v[172:175], v[136:139]
	ds_read_b128 v[200:203], v101 offset:2048
	v_mfma_f32_16x16x32_f16 v[140:143], v[192:195], v[172:175], v[140:143]
	ds_read_b128 v[204:207], v101 offset:4096
	v_mfma_f32_16x16x32_f16 v[144:147], v[184:187], v[176:179], v[144:147]
	ds_read_b128 v[208:211], v101 offset:6144
	v_mfma_f32_16x16x32_f16 v[148:151], v[188:191], v[176:179], v[148:151]
	v_mfma_f32_16x16x32_f16 v[152:155], v[192:195], v[176:179], v[152:155]
	v_mfma_f32_16x16x32_f16 v[156:159], v[184:187], v[180:183], v[156:159]
	v_mfma_f32_16x16x32_f16 v[160:163], v[188:191], v[180:183], v[160:163]
	v_mfma_f32_16x16x32_f16 v[164:167], v[192:195], v[180:183], v[164:167]
	s_waitcnt lgkmcnt(0)
	v_mfma_f32_16x16x32_f16 v[120:123], v[212:215], v[196:199], v[120:123]
	v_mfma_f32_16x16x32_f16 v[124:127], v[216:219], v[196:199], v[124:127]
	v_mfma_f32_16x16x32_f16 v[128:131], v[220:223], v[196:199], v[128:131]
	v_mfma_f32_16x16x32_f16 v[132:135], v[212:215], v[200:203], v[132:135]
	v_mfma_f32_16x16x32_f16 v[136:139], v[216:219], v[200:203], v[136:139]
	v_mfma_f32_16x16x32_f16 v[140:143], v[220:223], v[200:203], v[140:143]
	v_mfma_f32_16x16x32_f16 v[144:147], v[212:215], v[204:207], v[144:147]
	v_mfma_f32_16x16x32_f16 v[148:151], v[216:219], v[204:207], v[148:151]
	v_mfma_f32_16x16x32_f16 v[152:155], v[220:223], v[204:207], v[152:155]
	v_mfma_f32_16x16x32_f16 v[156:159], v[212:215], v[208:211], v[156:159]
	v_mfma_f32_16x16x32_f16 v[160:163], v[216:219], v[208:211], v[160:163]
	v_mfma_f32_16x16x32_f16 v[164:167], v[220:223], v[208:211], v[164:167]
.Lgk_loop_dn_done:
	s_nop 7
	s_nop 3
	v_bfe_u32 v96, v0, 4, 2
	v_lshlrev_b32_e32 v96, 2, v96
	s_add_i32 s2, s23, s0
	v_or_b32_e32 v98, s2, v96
	v_ashrrev_i32_e32 v99, 31, v98
	v_lshl_add_u64 v[98:99], v[98:99], 2, s[14:15]
	global_load_dwordx4 v[104:107], v[98:99], off
	global_load_dwordx4 v[108:111], v[98:99], off offset:64
	global_load_dwordx4 v[112:115], v[98:99], off offset:128
	s_movk_i32 s4, 0x310
	v_mul_lo_u32 v1, v1, s4
	v_or_b32_e32 v97, s23, v96
	v_lshlrev_b32_e32 v97, 2, v97
	v_add3_u32 v1, 0, v97, v1
	s_waitcnt lgkmcnt(0)
	s_barrier
	s_waitcnt vmcnt(0)
	v_pk_add_f32 v[120:121], v[104:105], v[120:121]
	v_pk_add_f32 v[122:123], v[106:107], v[122:123]
	ds_write_b128 v1, v[120:123] offset:0
	v_pk_add_f32 v[124:125], v[108:109], v[124:125]
	v_pk_add_f32 v[126:127], v[110:111], v[126:127]
	ds_write_b128 v1, v[124:127] offset:64
	v_pk_add_f32 v[128:129], v[112:113], v[128:129]
	v_pk_add_f32 v[130:131], v[114:115], v[130:131]
	ds_write_b128 v1, v[128:131] offset:128
	v_pk_add_f32 v[132:133], v[104:105], v[132:133]
	v_pk_add_f32 v[134:135], v[106:107], v[134:135]
	ds_write_b128 v1, v[132:135] offset:12544
	v_pk_add_f32 v[136:137], v[108:109], v[136:137]
	v_pk_add_f32 v[138:139], v[110:111], v[138:139]
	ds_write_b128 v1, v[136:139] offset:12608
	v_pk_add_f32 v[140:141], v[112:113], v[140:141]
	v_pk_add_f32 v[142:143], v[114:115], v[142:143]
	ds_write_b128 v1, v[140:143] offset:12672
	v_pk_add_f32 v[144:145], v[104:105], v[144:145]
	v_pk_add_f32 v[146:147], v[106:107], v[146:147]
	ds_write_b128 v1, v[144:147] offset:25088
	v_pk_add_f32 v[148:149], v[108:109], v[148:149]
	v_pk_add_f32 v[150:151], v[110:111], v[150:151]
	ds_write_b128 v1, v[148:151] offset:25152
	v_pk_add_f32 v[152:153], v[112:113], v[152:153]
	v_pk_add_f32 v[154:155], v[114:115], v[154:155]
	ds_write_b128 v1, v[152:155] offset:25216
	v_pk_add_f32 v[156:157], v[104:105], v[156:157]
	v_pk_add_f32 v[158:159], v[106:107], v[158:159]
	ds_write_b128 v1, v[156:159] offset:37632
	v_pk_add_f32 v[160:161], v[108:109], v[160:161]
	v_pk_add_f32 v[162:163], v[110:111], v[162:163]
	ds_write_b128 v1, v[160:163] offset:37696
	v_pk_add_f32 v[164:165], v[112:113], v[164:165]
	v_pk_add_f32 v[166:167], v[114:115], v[166:167]
	ds_write_b128 v1, v[164:167] offset:37760
	s_waitcnt lgkmcnt(0)
	s_barrier
	ds_read_b128 v[120:123], v38
	ds_read_b128 v[124:127], v39
	ds_read_b128 v[128:131], v40
	ds_read_b128 v[132:135], v41
	ds_read_b128 v[136:139], v42
	ds_read_b128 v[140:143], v43
	ds_read_b128 v[144:147], v44
	ds_read_b128 v[148:151], v45
	ds_read_b128 v[152:155], v46
	ds_read_b128 v[156:159], v47
	ds_read_b128 v[160:163], v48
	ds_read_b128 v[164:167], v49
	v_cvt_f32_f16_e32 v50, v2
	v_cvt_f32_f16_sdwa v51, v2 dst_sel:DWORD dst_unused:UNUSED_PAD src0_sel:WORD_1
	v_cvt_f32_f16_e32 v52, v3
	v_cvt_f32_f16_sdwa v53, v3 dst_sel:DWORD dst_unused:UNUSED_PAD src0_sel:WORD_1
	v_lshlrev_b32_e32 v26, 2, v26
	s_waitcnt lgkmcnt(11)
	v_pk_add_f32 v[120:121], v[120:121], v[50:51]
	v_pk_add_f32 v[122:123], v[122:123], v[52:53]
	global_store_dwordx4 v26, v[120:123], s[74:75] nt
	v_cvt_f32_f16_e32 v50, v4
	v_cvt_f32_f16_sdwa v51, v4 dst_sel:DWORD dst_unused:UNUSED_PAD src0_sel:WORD_1
	v_cvt_f32_f16_e32 v52, v5
	v_cvt_f32_f16_sdwa v53, v5 dst_sel:DWORD dst_unused:UNUSED_PAD src0_sel:WORD_1
	v_lshlrev_b32_e32 v27, 2, v27
	s_waitcnt lgkmcnt(10)
	v_pk_add_f32 v[124:125], v[124:125], v[50:51]
	v_pk_add_f32 v[126:127], v[126:127], v[52:53]
	global_store_dwordx4 v27, v[124:127], s[74:75] nt
	v_cvt_f32_f16_e32 v50, v6
	v_cvt_f32_f16_sdwa v51, v6 dst_sel:DWORD dst_unused:UNUSED_PAD src0_sel:WORD_1
	v_cvt_f32_f16_e32 v52, v7
	v_cvt_f32_f16_sdwa v53, v7 dst_sel:DWORD dst_unused:UNUSED_PAD src0_sel:WORD_1
	v_lshlrev_b32_e32 v28, 2, v28
	s_waitcnt lgkmcnt(9)
	v_pk_add_f32 v[128:129], v[128:129], v[50:51]
	v_pk_add_f32 v[130:131], v[130:131], v[52:53]
	global_store_dwordx4 v28, v[128:131], s[74:75] nt
	v_cvt_f32_f16_e32 v50, v8
	v_cvt_f32_f16_sdwa v51, v8 dst_sel:DWORD dst_unused:UNUSED_PAD src0_sel:WORD_1
	v_cvt_f32_f16_e32 v52, v9
	v_cvt_f32_f16_sdwa v53, v9 dst_sel:DWORD dst_unused:UNUSED_PAD src0_sel:WORD_1
	v_lshlrev_b32_e32 v29, 2, v29
	s_waitcnt lgkmcnt(8)
	v_pk_add_f32 v[132:133], v[132:133], v[50:51]
	v_pk_add_f32 v[134:135], v[134:135], v[52:53]
	global_store_dwordx4 v29, v[132:135], s[74:75] nt
	v_cvt_f32_f16_e32 v50, v10
	v_cvt_f32_f16_sdwa v51, v10 dst_sel:DWORD dst_unused:UNUSED_PAD src0_sel:WORD_1
	v_cvt_f32_f16_e32 v52, v11
	v_cvt_f32_f16_sdwa v53, v11 dst_sel:DWORD dst_unused:UNUSED_PAD src0_sel:WORD_1
	v_lshlrev_b32_e32 v30, 2, v30
	s_waitcnt lgkmcnt(7)
	v_pk_add_f32 v[136:137], v[136:137], v[50:51]
	v_pk_add_f32 v[138:139], v[138:139], v[52:53]
	global_store_dwordx4 v30, v[136:139], s[74:75] nt
	v_cvt_f32_f16_e32 v50, v12
	v_cvt_f32_f16_sdwa v51, v12 dst_sel:DWORD dst_unused:UNUSED_PAD src0_sel:WORD_1
	v_cvt_f32_f16_e32 v52, v13
	v_cvt_f32_f16_sdwa v53, v13 dst_sel:DWORD dst_unused:UNUSED_PAD src0_sel:WORD_1
	v_lshlrev_b32_e32 v31, 2, v31
	s_waitcnt lgkmcnt(6)
	v_pk_add_f32 v[140:141], v[140:141], v[50:51]
	v_pk_add_f32 v[142:143], v[142:143], v[52:53]
	global_store_dwordx4 v31, v[140:143], s[74:75] nt
	v_cvt_f32_f16_e32 v50, v14
	v_cvt_f32_f16_sdwa v51, v14 dst_sel:DWORD dst_unused:UNUSED_PAD src0_sel:WORD_1
	v_cvt_f32_f16_e32 v52, v15
	v_cvt_f32_f16_sdwa v53, v15 dst_sel:DWORD dst_unused:UNUSED_PAD src0_sel:WORD_1
	v_lshlrev_b32_e32 v32, 2, v32
	s_waitcnt lgkmcnt(5)
	v_pk_add_f32 v[144:145], v[144:145], v[50:51]
	v_pk_add_f32 v[146:147], v[146:147], v[52:53]
	global_store_dwordx4 v32, v[144:147], s[74:75] nt
	v_cvt_f32_f16_e32 v50, v16
	v_cvt_f32_f16_sdwa v51, v16 dst_sel:DWORD dst_unused:UNUSED_PAD src0_sel:WORD_1
	v_cvt_f32_f16_e32 v52, v17
	v_cvt_f32_f16_sdwa v53, v17 dst_sel:DWORD dst_unused:UNUSED_PAD src0_sel:WORD_1
	v_lshlrev_b32_e32 v33, 2, v33
	s_waitcnt lgkmcnt(4)
	v_pk_add_f32 v[148:149], v[148:149], v[50:51]
	v_pk_add_f32 v[150:151], v[150:151], v[52:53]
	global_store_dwordx4 v33, v[148:151], s[74:75] nt
	v_cvt_f32_f16_e32 v50, v18
	v_cvt_f32_f16_sdwa v51, v18 dst_sel:DWORD dst_unused:UNUSED_PAD src0_sel:WORD_1
	v_cvt_f32_f16_e32 v52, v19
	v_cvt_f32_f16_sdwa v53, v19 dst_sel:DWORD dst_unused:UNUSED_PAD src0_sel:WORD_1
	v_lshlrev_b32_e32 v34, 2, v34
	s_waitcnt lgkmcnt(3)
	v_pk_add_f32 v[152:153], v[152:153], v[50:51]
	v_pk_add_f32 v[154:155], v[154:155], v[52:53]
	global_store_dwordx4 v34, v[152:155], s[74:75] nt
	v_cvt_f32_f16_e32 v50, v20
	v_cvt_f32_f16_sdwa v51, v20 dst_sel:DWORD dst_unused:UNUSED_PAD src0_sel:WORD_1
	v_cvt_f32_f16_e32 v52, v21
	v_cvt_f32_f16_sdwa v53, v21 dst_sel:DWORD dst_unused:UNUSED_PAD src0_sel:WORD_1
	v_lshlrev_b32_e32 v35, 2, v35
	s_waitcnt lgkmcnt(2)
	v_pk_add_f32 v[156:157], v[156:157], v[50:51]
	v_pk_add_f32 v[158:159], v[158:159], v[52:53]
	global_store_dwordx4 v35, v[156:159], s[74:75] nt
	v_cvt_f32_f16_e32 v50, v22
	v_cvt_f32_f16_sdwa v51, v22 dst_sel:DWORD dst_unused:UNUSED_PAD src0_sel:WORD_1
	v_cvt_f32_f16_e32 v52, v23
	v_cvt_f32_f16_sdwa v53, v23 dst_sel:DWORD dst_unused:UNUSED_PAD src0_sel:WORD_1
	v_lshlrev_b32_e32 v36, 2, v36
	s_waitcnt lgkmcnt(1)
	v_pk_add_f32 v[160:161], v[160:161], v[50:51]
	v_pk_add_f32 v[162:163], v[162:163], v[52:53]
	global_store_dwordx4 v36, v[160:163], s[74:75] nt
	v_cvt_f32_f16_e32 v50, v24
	v_cvt_f32_f16_sdwa v51, v24 dst_sel:DWORD dst_unused:UNUSED_PAD src0_sel:WORD_1
	v_cvt_f32_f16_e32 v52, v25
	v_cvt_f32_f16_sdwa v53, v25 dst_sel:DWORD dst_unused:UNUSED_PAD src0_sel:WORD_1
	v_lshlrev_b32_e32 v37, 2, v37
	s_waitcnt lgkmcnt(0)
	v_pk_add_f32 v[164:165], v[164:165], v[50:51]
	v_pk_add_f32 v[166:167], v[166:167], v[52:53]
	global_store_dwordx4 v37, v[164:167], s[74:75] nt
	s_endpgm
	.p2align	8

	.amdhsa_kernel _Z6gemm_kILi1ELb1ELb1ELb0ELb0ELb1EEvPKtS1_ii7EpiArgs
		.amdhsa_group_segment_fixed_size 0
		.amdhsa_private_segment_fixed_size 0
		.amdhsa_kernarg_size 88
		.amdhsa_user_sgpr_count 2
		.amdhsa_user_sgpr_dispatch_ptr 0
		.amdhsa_user_sgpr_queue_ptr 0
		.amdhsa_user_sgpr_kernarg_segment_ptr 1
		.amdhsa_user_sgpr_dispatch_id 0
		.amdhsa_user_sgpr_kernarg_preload_length 0
		.amdhsa_user_sgpr_kernarg_preload_offset 0
		.amdhsa_user_sgpr_private_segment_size 0
		.amdhsa_uses_dynamic_stack 0
		.amdhsa_enable_private_segment 0
		.amdhsa_system_sgpr_workgroup_id_x 1
		.amdhsa_system_sgpr_workgroup_id_y 0
		.amdhsa_system_sgpr_workgroup_id_z 0
		.amdhsa_system_sgpr_workgroup_info 0
		.amdhsa_system_vgpr_workitem_id 0
		.amdhsa_next_free_vgpr 224
		.amdhsa_next_free_sgpr 78
		.amdhsa_accum_offset 224
		.amdhsa_reserve_vcc 0
		.amdhsa_float_round_mode_32 0
		.amdhsa_float_round_mode_16_64 0
		.amdhsa_float_denorm_mode_32 3
		.amdhsa_float_denorm_mode_16_64 3
		.amdhsa_dx10_clamp 1
		.amdhsa_ieee_mode 1
		.amdhsa_fp16_overflow 0
		.amdhsa_tg_split 0
		.amdhsa_exception_fp_ieee_invalid_op 0
		.amdhsa_exception_fp_denorm_src 0
		.amdhsa_exception_fp_ieee_div_zero 0
		.amdhsa_exception_fp_ieee_overflow 0
		.amdhsa_exception_fp_ieee_underflow 0
		.amdhsa_exception_fp_ieee_inexact 0
		.amdhsa_exception_int_div_zero 0
	.end_amdhsa_kernel

amdhsa.kernels:
  - .agpr_count:     0
    .args:
      - .offset:         0
        .size:           144
        .value_kind:     by_value
    .group_segment_fixed_size: 16640
    .kernarg_segment_align: 8
    .kernarg_segment_size: 144
    .language:       OpenCL C
    .language_version:
      - 2
      - 0
    .max_flat_workgroup_size: 256
    .name:           _Z8prep_ln18PrepArgs
    .private_segment_fixed_size: 0
    .sgpr_count:     18
    .sgpr_spill_count: 0
    .symbol:         _Z8prep_ln18PrepArgs.kd
    .uniform_work_group_size: 1
    .uses_dynamic_stack: false
    .vgpr_count:     61
    .vgpr_spill_count: 0
    .wavefront_size: 64
  - .agpr_count:     0
    .args:
      - .address_space:  global
        .offset:         0
        .size:           8
        .value_kind:     global_buffer
      - .address_space:  global
        .offset:         8
        .size:           8
        .value_kind:     global_buffer
      - .address_space:  global
        .offset:         16
        .size:           8
        .value_kind:     global_buffer
      - .address_space:  global
        .offset:         24
        .size:           8
        .value_kind:     global_buffer
      - .offset:         32
        .size:           144
        .value_kind:     by_value
    .group_segment_fixed_size: 0
    .kernarg_segment_align: 8
    .kernarg_segment_size: 176
    .language:       OpenCL C
    .language_version:
      - 2
      - 0
    .max_flat_workgroup_size: 256
    .name:           _Z10attn64_fwdPKtS0_S0_Pt8PrepArgs
    .private_segment_fixed_size: 0
    .sgpr_count:     42
    .sgpr_spill_count: 0
    .symbol:         _Z10attn64_fwdPKtS0_S0_Pt8PrepArgs.kd
    .uniform_work_group_size: 1
    .uses_dynamic_stack: false
    .vgpr_count:     221
    .vgpr_spill_count: 0
    .wavefront_size: 64
  - .agpr_count:     0
    .args:
      - .address_space:  global
        .offset:         0
        .size:           8
        .value_kind:     global_buffer
      - .address_space:  global
        .offset:         8
        .size:           8
        .value_kind:     global_buffer
      - .offset:         16
        .size:           4
        .value_kind:     by_value
      - .offset:         20
        .size:           4
        .value_kind:     by_value
      - .offset:         24
        .size:           64
        .value_kind:     by_value
    .group_segment_fixed_size: 0
    .kernarg_segment_align: 8
    .kernarg_segment_size: 88
    .language:       OpenCL C
    .language_version:
      - 2
      - 0
    .max_flat_workgroup_size: 256
    .name:           _Z8gemm2b_kILi2EEvPKtS1_ii7EpiArgs
    .private_segment_fixed_size: 0
    .sgpr_count:     75
    .sgpr_spill_count: 0
    .symbol:         _Z8gemm2b_kILi2EEvPKtS1_ii7EpiArgs.kd
    .uniform_work_group_size: 1
    .uses_dynamic_stack: false
    .vgpr_count:     182
    .vgpr_spill_count: 0
    .wavefront_size: 64
  - .agpr_count:     0
    .args:
      - .address_space:  global
        .offset:         0
        .size:           8
        .value_kind:     global_buffer
      - .address_space:  global
        .offset:         8
        .size:           8
        .value_kind:     global_buffer
      - .offset:         16
        .size:           4
        .value_kind:     by_value
      - .offset:         20
        .size:           4
        .value_kind:     by_value
      - .offset:         24
        .size:           64
        .value_kind:     by_value
    .group_segment_fixed_size: 0
    .kernarg_segment_align: 8
    .kernarg_segment_size: 88
    .language:       OpenCL C
    .language_version:
      - 2
      - 0
    .max_flat_workgroup_size: 256
    .name:           _Z8gemm2b_kILi0EEvPKtS1_ii7EpiArgs
    .private_segment_fixed_size: 0
    .sgpr_count:     85
    .sgpr_spill_count: 0
    .symbol:         _Z8gemm2b_kILi0EEvPKtS1_ii7EpiArgs.kd
    .uniform_work_group_size: 1
    .uses_dynamic_stack: false
    .vgpr_count:     186
    .vgpr_spill_count: 0
    .wavefront_size: 64
  - .agpr_count:     0
    .args:
      - .address_space:  global
        .offset:         0
        .size:           8
        .value_kind:     global_buffer
      - .address_space:  global
        .offset:         8
        .size:           8
        .value_kind:     global_buffer
      - .offset:         16
        .size:           4
        .value_kind:     by_value
      - .offset:         20
        .size:           4
        .value_kind:     by_value
      - .offset:         24
        .size:           64
        .value_kind:     by_value
    .group_segment_fixed_size: 0
    .kernarg_segment_align: 8
    .kernarg_segment_size: 88
    .language:       OpenCL C
    .language_version:
      - 2
      - 0
    .max_flat_workgroup_size: 512
    .name:           _Z6gemm_kILi1ELb1ELb0ELb1ELb1ELb0EEvPKtS1_ii7EpiArgs
    .private_segment_fixed_size: 0
    .sgpr_count:     61
    .sgpr_spill_count: 0
    .symbol:         _Z6gemm_kILi1ELb1ELb0ELb1ELb1ELb0EEvPKtS1_ii7EpiArgs.kd
    .uniform_work_group_size: 1
    .uses_dynamic_stack: false
    .vgpr_count:     116
    .vgpr_spill_count: 0
    .wavefront_size: 64
  - .agpr_count:     0
    .args:
      - .address_space:  global
        .offset:         0
        .size:           8
        .value_kind:     global_buffer
      - .address_space:  global
        .offset:         8
        .size:           8
        .value_kind:     global_buffer
      - .offset:         16
        .size:           4
        .value_kind:     by_value
      - .offset:         20
        .size:           4
        .value_kind:     by_value
      - .offset:         24
        .size:           64
        .value_kind:     by_value
    .group_segment_fixed_size: 0
    .kernarg_segment_align: 8
    .kernarg_segment_size: 88
    .language:       OpenCL C
    .language_version:
      - 2
      - 0
    .max_flat_workgroup_size: 512
    .name:           _Z6gemm_kILi1ELb1ELb1ELb0ELb0ELb1EEvPKtS1_ii7EpiArgs
    .private_segment_fixed_size: 0
    .sgpr_count:     84
    .sgpr_spill_count: 0
    .symbol:         _Z6gemm_kILi1ELb1ELb1ELb0ELb0ELb1EEvPKtS1_ii7EpiArgs.kd
    .uniform_work_group_size: 1
    .uses_dynamic_stack: false
    .vgpr_count:     224
    .vgpr_spill_count: 0
    .wavefront_size: 64
